# P5 out-proj epilogue: the 16 serialized x-load round trips per unit batched into 2 (all x loads issued before any store); NA bias loads batched ahead of K/V prefetch; P0 ticket
# speedup vs baseline: 1.0195x; 1.0106x over previous
; __device__ __forceinline__ float bflo(unsigned w) { return __uint_as_float(w << 16); }
; __device__ __forceinline__ float bfhi(unsigned w) { return __uint_as_float(w & 0xffff0000u); }
;     __device__ __forceinline__ void operator()(const f32x4 (&acc)[2][2][4][2], const Unit& u, int wr, int wc, int fr, int fq) const {
;         const int row0 = u.pm * BM + (u.hf == 2 ? HALF : 0) + wr * 64 + fr, col0 = u.pc * BM + wc * 32 + 8 * fq;
;         const int mrow = u.pm < 64 ? (u.pm >> 4) : 4;
;         f32x4 gv[2][2];
; #pragma unroll
;         for (int bj = 0; bj < 2; ++bj)
; #pragma unroll
;             for (int n = 0; n < 2; ++n) gv[bj][n] = *(const f32x4*)(g1 + (size_t)mrow * 12288 + col0 + bj * HALF + 4 * n);
; #pragma unroll
;         for (int ai = 0; ai < 2; ++ai) if (ai == 0 || u.hf == 0)
; #pragma unroll
;             for (int m = 0; m < 4; ++m) { const int row = row0 + ai * HALF + m * 16;
;                 bf16_t* orow = X1 + (size_t)row * D + col0;
; #pragma unroll
;                 for (int bj = 0; bj < 2; ++bj) { f32x4 x0, x1;
;                     if (XIN_BF16) { const u32x4 w = *(const u32x4*)(orow + bj * HALF); x0 = (f32x4){bflo(w.x), bfhi(w.x), bflo(w.y), bfhi(w.y)}; x1 = (f32x4){bflo(w.z), bfhi(w.z), bflo(w.w), bfhi(w.w)}; }
;                     else { const float* xr = (u.pm < 64 ? xinLat + (size_t)row * D : xinCtx + (size_t)(row - M_LAT) * D) + col0 + bj * HALF; x0 = *(const f32x4*)xr; x1 = *(const f32x4*)(xr + 4); }
;                     const f32x4 v0 = x0 + gv[bj][0] * acc[ai][bj][m][0], v1 = x1 + gv[bj][1] * acc[ai][bj][m][1];
;                     u32x4 w; w.x = pk2(v0[0], v0[1]); w.y = pk2(v0[2], v0[3]); w.z = pk2(v1[0], v1[1]); w.w = pk2(v1[2], v1[3]);
;                     *(u32x4*)(orow + bj * HALF) = w; } }
.LBB0_529:
	s_lshl_b32 s4, s26, 8
	s_cmp_eq_u32 s61, 2
	s_cselect_b32 s5, 0x80, 0
	s_waitcnt lgkmcnt(0)
	v_lshl_or_b32 v132, s24, 8, v227
	s_lshl_b64 s[2:3], s[2:3], 2
	s_add_u32 s2, s52, s2
	v_ashrrev_i32_e32 v133, 31, v132
	s_addc_u32 s3, s53, s3
	v_lshlrev_b64 v[148:149], 2, v[132:133]
	v_lshl_add_u64 v[136:137], s[2:3], 0, v[148:149]
	s_or_b32 s2, s4, s5
	v_add_u32_e32 v150, s2, v1
	v_ashrrev_i32_e32 v151, 31, v150
	v_readlane_b32 s68, v254, 5
	v_lshlrev_b64 v[134:135], 13, v[150:151]
	v_readlane_b32 s72, v254, 9
	v_readlane_b32 s73, v254, 10
	s_brev_b32 s2, 31
	v_readlane_b32 s69, v254, 6
	v_lshl_add_u64 v[154:155], s[72:73], 0, v[134:135]
	s_mov_b32 s3, -1
	v_lshl_add_u64 v[138:139], s[68:69], 0, v[134:135]
	v_lshl_add_u64 v[134:135], v[154:155], 0, s[2:3]
	v_cndmask_b32_e32 v135, v135, v139, vcc
	v_cndmask_b32_e32 v134, v134, v138, vcc
	v_lshl_add_u64 v[164:165], v[134:135], 0, v[148:149]
	v_readlane_b32 s4, v255, 5
	v_lshlrev_b64 v[166:167], 12, v[150:151]
	v_readlane_b32 s5, v255, 6
	v_lshlrev_b64 v[152:153], 1, v[132:133]
	s_mov_b64 s[64:65], 0x20000
	s_mov_b64 s[66:67], 0x10000
	global_load_dwordx4 v[144:147], v[136:137], off
	global_load_dwordx4 v[140:143], v[136:137], off offset:16
	global_load_dwordx4 v[132:135], v[136:137], off offset:528
	s_nop 0
	global_load_dwordx4 v[136:139], v[136:137], off offset:512
	v_lshl_add_u64 v[166:167], s[4:5], 0, v[166:167]
	v_lshl_add_u64 v[166:167], v[166:167], 0, v[152:153]
	global_load_dwordx4 v[168:171], v[164:165], off
	global_load_dwordx4 v[172:175], v[164:165], off offset:16
	global_load_dwordx4 v[176:179], v[164:165], off offset:512
	global_load_dwordx4 v[180:183], v[164:165], off offset:528
	v_lshl_add_u64 v[164:165], v[164:165], 0, s[64:65]
	global_load_dwordx4 v[184:187], v[164:165], off
	global_load_dwordx4 v[188:191], v[164:165], off offset:16
	global_load_dwordx4 v[192:195], v[164:165], off offset:512
	global_load_dwordx4 v[214:217], v[164:165], off offset:528
	v_lshl_add_u64 v[164:165], v[164:165], 0, s[64:65]
	global_load_dwordx4 v[218:221], v[164:165], off
	global_load_dwordx4 v[222:225], v[164:165], off offset:16
	global_load_dwordx4 v[234:237], v[164:165], off offset:512
	global_load_dwordx4 v[238:241], v[164:165], off offset:528
	v_lshl_add_u64 v[164:165], v[164:165], 0, s[64:65]
	global_load_dwordx4 v[242:245], v[164:165], off
	global_load_dwordx4 v[246:249], v[164:165], off offset:16
	global_load_dwordx4 v[250:253], v[164:165], off offset:512
	global_load_dwordx4 v[156:159], v[164:165], off offset:528
	v_readlane_b32 s70, v254, 7
	v_readlane_b32 s71, v254, 8
	v_readlane_b32 s74, v254, 11
	v_readlane_b32 s75, v254, 12
	v_readlane_b32 s76, v254, 13
	v_readlane_b32 s77, v254, 14
	v_readlane_b32 s78, v254, 15
	v_readlane_b32 s79, v254, 16
	v_readlane_b32 s80, v254, 17
	v_readlane_b32 s81, v254, 18
	v_readlane_b32 s82, v254, 19
	v_readlane_b32 s83, v254, 20
	s_waitcnt vmcnt(12)
	v_pk_fma_f32 v[130:131], v[130:131], v[146:147], v[170:171]
	v_pk_fma_f32 v[128:129], v[128:129], v[144:145], v[168:169]
	v_pk_fma_f32 v[126:127], v[126:127], v[142:143], v[174:175]
	v_pk_fma_f32 v[124:125], v[124:125], v[140:141], v[172:173]
	v_cvt_pk_bf16_f32 v168, v128, v129
	v_cvt_pk_bf16_f32 v169, v130, v131
	v_cvt_pk_bf16_f32 v170, v124, v125
	v_cvt_pk_bf16_f32 v171, v126, v127
	global_store_dwordx4 v[166:167], v[168:171], off
	v_pk_fma_f32 v[118:119], v[118:119], v[138:139], v[178:179]
	v_pk_fma_f32 v[116:117], v[116:117], v[136:137], v[176:177]
	v_pk_fma_f32 v[110:111], v[110:111], v[134:135], v[182:183]
	v_pk_fma_f32 v[108:109], v[108:109], v[132:133], v[180:181]
	v_cvt_pk_bf16_f32 v176, v116, v117
	v_cvt_pk_bf16_f32 v177, v118, v119
	v_cvt_pk_bf16_f32 v178, v108, v109
	v_cvt_pk_bf16_f32 v179, v110, v111
	global_store_dwordx4 v[166:167], v[176:179], off offset:256
	v_lshl_add_u64 v[166:167], v[166:167], 0, s[66:67]
	s_waitcnt vmcnt(10)
	v_pk_fma_f32 v[122:123], v[122:123], v[146:147], v[186:187]
	v_pk_fma_f32 v[120:121], v[120:121], v[144:145], v[184:185]
	v_pk_fma_f32 v[114:115], v[114:115], v[142:143], v[190:191]
	v_pk_fma_f32 v[112:113], v[112:113], v[140:141], v[188:189]
	v_cvt_pk_bf16_f32 v184, v120, v121
	v_cvt_pk_bf16_f32 v185, v122, v123
	v_cvt_pk_bf16_f32 v186, v112, v113
	v_cvt_pk_bf16_f32 v187, v114, v115
	global_store_dwordx4 v[166:167], v[184:187], off
	v_pk_fma_f32 v[102:103], v[102:103], v[138:139], v[194:195]
	v_pk_fma_f32 v[100:101], v[100:101], v[136:137], v[192:193]
	v_pk_fma_f32 v[94:95], v[94:95], v[134:135], v[216:217]
	v_pk_fma_f32 v[92:93], v[92:93], v[132:133], v[214:215]
	v_cvt_pk_bf16_f32 v192, v100, v101
	v_cvt_pk_bf16_f32 v193, v102, v103
	v_cvt_pk_bf16_f32 v194, v92, v93
	v_cvt_pk_bf16_f32 v195, v94, v95
	global_store_dwordx4 v[166:167], v[192:195], off offset:256
	v_lshl_add_u64 v[166:167], v[166:167], 0, s[66:67]
	s_waitcnt vmcnt(8)
	v_pk_fma_f32 v[106:107], v[106:107], v[146:147], v[220:221]
	v_pk_fma_f32 v[104:105], v[104:105], v[144:145], v[218:219]
	v_pk_fma_f32 v[98:99], v[98:99], v[142:143], v[224:225]
	v_pk_fma_f32 v[96:97], v[96:97], v[140:141], v[222:223]
	v_cvt_pk_bf16_f32 v218, v104, v105
	v_cvt_pk_bf16_f32 v219, v106, v107
	v_cvt_pk_bf16_f32 v220, v96, v97
	v_cvt_pk_bf16_f32 v221, v98, v99
	global_store_dwordx4 v[166:167], v[218:221], off
	v_pk_fma_f32 v[86:87], v[86:87], v[138:139], v[236:237]
	v_pk_fma_f32 v[84:85], v[84:85], v[136:137], v[234:235]
	v_pk_fma_f32 v[82:83], v[82:83], v[134:135], v[240:241]
	v_pk_fma_f32 v[80:81], v[80:81], v[132:133], v[238:239]
	v_cvt_pk_bf16_f32 v234, v84, v85
	v_cvt_pk_bf16_f32 v235, v86, v87
	v_cvt_pk_bf16_f32 v236, v80, v81
	v_cvt_pk_bf16_f32 v237, v82, v83
	global_store_dwordx4 v[166:167], v[234:237], off offset:256
	v_lshl_add_u64 v[166:167], v[166:167], 0, s[66:67]
	s_waitcnt vmcnt(6)
	v_pk_fma_f32 v[90:91], v[90:91], v[146:147], v[244:245]
	v_pk_fma_f32 v[88:89], v[88:89], v[144:145], v[242:243]
	v_pk_fma_f32 v[78:79], v[78:79], v[142:143], v[248:249]
	v_pk_fma_f32 v[76:77], v[76:77], v[140:141], v[246:247]
	v_cvt_pk_bf16_f32 v242, v88, v89
	v_cvt_pk_bf16_f32 v243, v90, v91
	v_cvt_pk_bf16_f32 v244, v76, v77
	v_cvt_pk_bf16_f32 v245, v78, v79
	global_store_dwordx4 v[166:167], v[242:245], off
	v_pk_fma_f32 v[74:75], v[74:75], v[138:139], v[252:253]
	v_pk_fma_f32 v[72:73], v[72:73], v[136:137], v[250:251]
	v_pk_fma_f32 v[70:71], v[70:71], v[134:135], v[158:159]
	v_pk_fma_f32 v[68:69], v[68:69], v[132:133], v[156:157]
	v_cvt_pk_bf16_f32 v250, v72, v73
	v_cvt_pk_bf16_f32 v251, v74, v75
	v_cvt_pk_bf16_f32 v252, v68, v69
	v_cvt_pk_bf16_f32 v253, v70, v71
	global_store_dwordx4 v[166:167], v[250:253], off offset:256
	s_cmp_lg_u32 s61, 0
	s_cbranch_scc0 .LBB0_556

; __device__ __forceinline__ float bflo(unsigned w) { return __uint_as_float(w << 16); }
; __device__ __forceinline__ float bfhi(unsigned w) { return __uint_as_float(w & 0xffff0000u); }
;     __device__ __forceinline__ void operator()(const f32x4 (&acc)[2][2][4][2], const Unit& u, int wr, int wc, int fr, int fq) const {
;     ...
;         for (int ai = 0; ai < 2; ++ai) if (ai == 0 || u.hf == 0)
; #pragma unroll
;             for (int m = 0; m < 4; ++m) { const int row = row0 + ai * HALF + m * 16;
;                 bf16_t* orow = X1 + (size_t)row * D + col0;
; #pragma unroll
;                 for (int bj = 0; bj < 2; ++bj) { f32x4 x0, x1;
;                     if (XIN_BF16) { const u32x4 w = *(const u32x4*)(orow + bj * HALF); x0 = (f32x4){bflo(w.x), bfhi(w.x), bflo(w.y), bfhi(w.y)}; x1 = (f32x4){bflo(w.z), bfhi(w.z), bflo(w.w), bfhi(w.w)}; }
;                     else { const float* xr = (u.pm < 64 ? xinLat + (size_t)row * D : xinCtx + (size_t)(row - M_LAT) * D) + col0 + bj * HALF; x0 = *(const f32x4*)xr; x1 = *(const f32x4*)(xr + 4); }
;                     const f32x4 v0 = x0 + gv[bj][0] * acc[ai][bj][m][0], v1 = x1 + gv[bj][1] * acc[ai][bj][m][1];
;                     u32x4 w; w.x = pk2(v0[0], v0[1]); w.y = pk2(v0[2], v0[3]); w.z = pk2(v1[0], v1[1]); w.w = pk2(v1[2], v1[3]);
;                     *(u32x4*)(orow + bj * HALF) = w; } }
.LBB0_556:
	v_add_u32_e32 v76, 0x80, v150
	v_ashrrev_i32_e32 v77, 31, v76
	v_readlane_b32 s68, v254, 5
	s_mov_b32 s2, 0xf8100000
	v_lshlrev_b64 v[68:69], 13, v[76:77]
	v_readlane_b32 s69, v254, 6
	s_mov_b32 s3, -1
	v_lshl_add_u64 v[70:71], v[154:155], 0, s[2:3]
	v_lshl_add_u64 v[68:69], s[68:69], 0, v[68:69]
	v_cndmask_b32_e32 v69, v71, v69, vcc
	v_cndmask_b32_e32 v68, v70, v68, vcc
	v_lshl_add_u64 v[78:79], v[68:69], 0, v[148:149]
	v_readlane_b32 s4, v255, 5
	v_lshlrev_b64 v[76:77], 12, v[76:77]
	v_readlane_b32 s5, v255, 6
	s_mov_b64 s[64:65], 0x20000
	s_mov_b64 s[66:67], 0x10000
	global_load_dwordx4 v[168:171], v[78:79], off
	global_load_dwordx4 v[172:175], v[78:79], off offset:16
	global_load_dwordx4 v[176:179], v[78:79], off offset:512
	global_load_dwordx4 v[180:183], v[78:79], off offset:528
	v_lshl_add_u64 v[78:79], v[78:79], 0, s[64:65]
	global_load_dwordx4 v[184:187], v[78:79], off
	global_load_dwordx4 v[188:191], v[78:79], off offset:16
	global_load_dwordx4 v[192:195], v[78:79], off offset:512
	global_load_dwordx4 v[214:217], v[78:79], off offset:528
	v_lshl_add_u64 v[78:79], v[78:79], 0, s[64:65]
	global_load_dwordx4 v[218:221], v[78:79], off
	global_load_dwordx4 v[222:225], v[78:79], off offset:16
	global_load_dwordx4 v[234:237], v[78:79], off offset:512
	global_load_dwordx4 v[238:241], v[78:79], off offset:528
	v_lshl_add_u64 v[78:79], v[78:79], 0, s[64:65]
	global_load_dwordx4 v[242:245], v[78:79], off
	global_load_dwordx4 v[246:249], v[78:79], off offset:16
	global_load_dwordx4 v[250:253], v[78:79], off offset:512
	global_load_dwordx4 v[104:107], v[78:79], off offset:528
	v_lshl_add_u64 v[76:77], s[4:5], 0, v[76:77]
	v_lshl_add_u64 v[76:77], v[76:77], 0, v[152:153]
	v_readlane_b32 s70, v254, 7
	v_readlane_b32 s71, v254, 8
	v_readlane_b32 s72, v254, 9
	v_readlane_b32 s73, v254, 10
	v_readlane_b32 s74, v254, 11
	v_readlane_b32 s75, v254, 12
	v_readlane_b32 s76, v254, 13
	v_readlane_b32 s77, v254, 14
	v_readlane_b32 s78, v254, 15
	v_readlane_b32 s79, v254, 16
	v_readlane_b32 s80, v254, 17
	v_readlane_b32 s81, v254, 18
	v_readlane_b32 s82, v254, 19
	v_readlane_b32 s83, v254, 20
	s_waitcnt vmcnt(12)
	v_pk_fma_f32 v[66:67], v[66:67], v[146:147], v[170:171]
	v_pk_fma_f32 v[64:65], v[64:65], v[144:145], v[168:169]
	v_pk_fma_f32 v[62:63], v[62:63], v[142:143], v[174:175]
	v_pk_fma_f32 v[60:61], v[60:61], v[140:141], v[172:173]
	v_cvt_pk_bf16_f32 v168, v64, v65
	v_cvt_pk_bf16_f32 v169, v66, v67
	v_cvt_pk_bf16_f32 v170, v60, v61
	v_cvt_pk_bf16_f32 v171, v62, v63
	global_store_dwordx4 v[76:77], v[168:171], off
	v_pk_fma_f32 v[58:59], v[58:59], v[138:139], v[178:179]
	v_pk_fma_f32 v[56:57], v[56:57], v[136:137], v[176:177]
	v_pk_fma_f32 v[54:55], v[54:55], v[134:135], v[182:183]
	v_pk_fma_f32 v[52:53], v[52:53], v[132:133], v[180:181]
	v_cvt_pk_bf16_f32 v176, v56, v57
	v_cvt_pk_bf16_f32 v177, v58, v59
	v_cvt_pk_bf16_f32 v178, v52, v53
	v_cvt_pk_bf16_f32 v179, v54, v55
	global_store_dwordx4 v[76:77], v[176:179], off offset:256
	v_lshl_add_u64 v[76:77], v[76:77], 0, s[66:67]
	s_waitcnt vmcnt(10)
	v_pk_fma_f32 v[50:51], v[50:51], v[146:147], v[186:187]
	v_pk_fma_f32 v[48:49], v[48:49], v[144:145], v[184:185]
	v_pk_fma_f32 v[46:47], v[46:47], v[142:143], v[190:191]
	v_pk_fma_f32 v[44:45], v[44:45], v[140:141], v[188:189]
	v_cvt_pk_bf16_f32 v184, v48, v49
	v_cvt_pk_bf16_f32 v185, v50, v51
	v_cvt_pk_bf16_f32 v186, v44, v45
	v_cvt_pk_bf16_f32 v187, v46, v47
	global_store_dwordx4 v[76:77], v[184:187], off
	v_pk_fma_f32 v[42:43], v[42:43], v[138:139], v[194:195]
	v_pk_fma_f32 v[40:41], v[40:41], v[136:137], v[192:193]
	v_pk_fma_f32 v[38:39], v[38:39], v[134:135], v[216:217]
	v_pk_fma_f32 v[36:37], v[36:37], v[132:133], v[214:215]
	v_cvt_pk_bf16_f32 v192, v40, v41
	v_cvt_pk_bf16_f32 v193, v42, v43
	v_cvt_pk_bf16_f32 v194, v36, v37
	v_cvt_pk_bf16_f32 v195, v38, v39
	global_store_dwordx4 v[76:77], v[192:195], off offset:256
	v_lshl_add_u64 v[76:77], v[76:77], 0, s[66:67]
	s_waitcnt vmcnt(8)
	v_pk_fma_f32 v[34:35], v[34:35], v[146:147], v[220:221]
	v_pk_fma_f32 v[32:33], v[32:33], v[144:145], v[218:219]
	v_pk_fma_f32 v[30:31], v[30:31], v[142:143], v[224:225]
	v_pk_fma_f32 v[28:29], v[28:29], v[140:141], v[222:223]
	v_cvt_pk_bf16_f32 v218, v32, v33
	v_cvt_pk_bf16_f32 v219, v34, v35
	v_cvt_pk_bf16_f32 v220, v28, v29
	v_cvt_pk_bf16_f32 v221, v30, v31
	global_store_dwordx4 v[76:77], v[218:221], off
	v_pk_fma_f32 v[26:27], v[26:27], v[138:139], v[236:237]
	v_pk_fma_f32 v[24:25], v[24:25], v[136:137], v[234:235]
	v_pk_fma_f32 v[22:23], v[22:23], v[134:135], v[240:241]
	v_pk_fma_f32 v[20:21], v[20:21], v[132:133], v[238:239]
	v_cvt_pk_bf16_f32 v234, v24, v25
	v_cvt_pk_bf16_f32 v235, v26, v27
	v_cvt_pk_bf16_f32 v236, v20, v21
	v_cvt_pk_bf16_f32 v237, v22, v23
	global_store_dwordx4 v[76:77], v[234:237], off offset:256
	v_lshl_add_u64 v[76:77], v[76:77], 0, s[66:67]
	s_waitcnt vmcnt(6)
	v_pk_fma_f32 v[18:19], v[18:19], v[146:147], v[244:245]
	v_pk_fma_f32 v[16:17], v[16:17], v[144:145], v[242:243]
	v_pk_fma_f32 v[14:15], v[14:15], v[142:143], v[248:249]
	v_pk_fma_f32 v[12:13], v[12:13], v[140:141], v[246:247]
	v_cvt_pk_bf16_f32 v242, v16, v17
	v_cvt_pk_bf16_f32 v243, v18, v19
	v_cvt_pk_bf16_f32 v244, v12, v13
	v_cvt_pk_bf16_f32 v245, v14, v15
	global_store_dwordx4 v[76:77], v[242:245], off
	v_pk_fma_f32 v[10:11], v[10:11], v[138:139], v[252:253]
	v_pk_fma_f32 v[8:9], v[8:9], v[136:137], v[250:251]
	v_pk_fma_f32 v[6:7], v[6:7], v[134:135], v[106:107]
	v_pk_fma_f32 v[4:5], v[4:5], v[132:133], v[104:105]
	v_cvt_pk_bf16_f32 v250, v8, v9
	v_cvt_pk_bf16_f32 v251, v10, v11
	v_cvt_pk_bf16_f32 v252, v4, v5
	v_cvt_pk_bf16_f32 v253, v6, v7
	global_store_dwordx4 v[76:77], v[250:253], off offset:256
	s_branch .LBB0_530

; #define LAS __attribute__((address_space(3)))
; #define NA_STORE(bufp) do { _Pragma("unroll") for (int i_ = 0; i_ < 4; ++i_) { const int id = tid + 512 * i_, key = id >> 4, ch = id & 15; \
;         *(LAS u32x4*)((bufp) + NA_KB + key * NA_RSK + ch * 16) = rk[i_]; *(LAS u32x4*)((bufp) + NA_VB + key * NA_RSV + ch * 16) = rv[i_]; } } while (0)
; __device__ __forceinline__ void na_fast_unit(int unit, const bf16_t* P, const float* rpb, bf16_t* AO, LAS unsigned char* lds) {
;     const int tid = threadIdx.x, lane = tid & 63, wv = __builtin_amdgcn_readfirstlane(tid >> 6);
;     const int cq = wv & 3, kh = wv >> 2;
;     const int r = unit & 63, h = (unit >> 6) & 7, b = unit >> 9;
;     const int l15 = lane & 15, q = lane >> 4, trq = l15 >> 2, trp = lane & 3;
;     const int rstart = min(max(r - 4, 0), 56);
;     const int col = 16 * cq + l15, cstart = min(max(col - 8, 0), 48);
;     const int ct0 = min(max(cq - 1, 0), 1);
;     const float scale = 0.08838834764831845f;
;     bf16x8 qf[4];
;     { const bf16_t* qp = P + (size_t)(b * T + r * 64 + col) * LDP1 + h * 128 + 8 * q;
; #pragma unroll
;         for (int kk = 0; kk < 4; ++kk) qf[kk] = *(const bf16x8*)(qp + 32 * kk); }
;     u32x4 rk[4], rv[4];
;     ...
;     float m = -1.0e30f, l = 0.f;
;     f32x4 accO[8];
; #pragma unroll
;     for (int c = 0; c < 8; ++c) accO[c] = (f32x4){0.f, 0.f, 0.f, 0.f};
;     __syncthreads();
;     NA_LOAD(0); NA_STORE(lds);
;     __syncthreads();
;     for (int s = 0; s < 6; ++s) {
;         LAS unsigned char* buf = lds + (s & 1) * NA_BUF;
;         if (s + 1 < 6) NA_LOAD(s + 1);
.LBB0_1213:
	s_or_b64 exec, exec, s[2:3]
	s_waitcnt lgkmcnt(0)
	s_barrier
	ds_read_b32 v2, v125
	s_movk_i32 s2, 0x7ff
	s_waitcnt lgkmcnt(0)
	v_cmp_lt_u32_e32 vcc, s2, v2
	v_readfirstlane_b32 s6, v2
	s_mov_b64 s[2:3], -1
	s_cbranch_vccnz .LBB0_1208
	s_and_b32 s16, s6, 63
	s_lshr_b32 s53, s6, 9
	v_readfirstlane_b32 s50, v0
	v_sub_u32_e64 v2, s16, 4 clamp
	s_lshl_b32 s54, s53, 12
	s_lshl_b32 s2, s16, 6
	s_bfe_u32 s51, s50, 0x20006
	s_or_b32 s49, s54, s2
	v_readfirstlane_b32 s2, v2
	s_lshl_b32 s48, s51, 4
	s_min_u32 s55, s2, 56
	s_bfe_u32 s56, s6, 0x30006
	v_or_b32_e32 v50, s48, v1
	s_lshl_b32 s6, s55, 6
	s_or_b32 s2, s54, s6
	v_or_b32_e32 v2, s49, v50
	s_movk_i32 s3, 0x1900
	v_readlane_b32 s18, v254, 61
	v_mul_lo_u32 v86, v2, s3
	v_readlane_b32 s19, v254, 62
	v_or_b32_e32 v18, s2, v168
	s_lshl_b32 s24, s56, 8
	v_lshl_add_u64 v[2:3], v[86:87], 1, s[18:19]
	v_mul_lo_u32 v86, v18, s46
	v_lshl_add_u64 v[18:19], s[18:19], 0, v[86:87]
	v_mov_b64_e32 v[42:43], s[18:19]
	v_lshl_add_u64 v[18:19], v[18:19], 0, s[24:25]
	v_mov_b32_e32 v93, v87
	v_or_b32_e32 v26, s2, v170
	v_or_b32_e32 v178, s54, v104
	v_lshl_add_u64 v[18:19], v[18:19], 0, v[92:93]
	v_mad_u64_u32 v[26:27], s[2:3], v26, s46, v[42:43]
	v_add_u32_e32 v34, s6, v178
	v_lshl_add_u64 v[22:23], v[18:19], 0, s[10:11]
	v_add_co_u32_e32 v18, vcc, s47, v18
	v_lshl_add_u64 v[26:27], v[26:27], 0, s[24:25]
	v_mul_lo_u32 v86, v34, s46
	v_add_u32_e64 v44, s55, 1
	v_addc_co_u32_e32 v19, vcc, 0, v19, vcc
	v_lshl_add_u64 v[26:27], v[26:27], 0, v[92:93]
	v_lshl_add_u64 v[34:35], s[18:19], 0, v[86:87]
	v_lshl_add_u32 v44, v44, 6, s54
	v_lshl_add_u64 v[30:31], v[26:27], 0, s[10:11]
	v_add_co_u32_e32 v26, vcc, s47, v26
	v_lshl_add_u64 v[34:35], v[34:35], 0, s[24:25]
	v_or_b32_e32 v44, v44, v106
	v_addc_co_u32_e32 v27, vcc, 0, v27, vcc
	v_lshl_add_u64 v[34:35], v[34:35], 0, v[92:93]
	v_mad_u64_u32 v[42:43], s[2:3], v44, s46, v[42:43]
	v_lshl_add_u64 v[38:39], v[34:35], 0, s[10:11]
	v_add_co_u32_e32 v34, vcc, s47, v34
	v_lshl_add_u64 v[42:43], v[42:43], 0, s[24:25]
	s_nop 0
	v_addc_co_u32_e32 v35, vcc, 0, v35, vcc
	v_lshl_add_u64 v[42:43], v[42:43], 0, v[92:93]
	v_lshl_add_u64 v[2:3], v[2:3], 0, s[24:25]
	v_mov_b32_e32 v91, v87
	v_lshl_add_u64 v[46:47], v[42:43], 0, s[10:11]
	v_add_co_u32_e32 v42, vcc, s47, v42
	v_lshl_add_u64 v[2:3], v[2:3], 0, v[90:91]
	s_nop 0
	v_addc_co_u32_e32 v43, vcc, 0, v43, vcc
	global_load_dwordx4 v[14:17], v[2:3], off
	global_load_dwordx4 v[10:13], v[2:3], off offset:64
	global_load_dwordx4 v[6:9], v[2:3], off offset:128
	s_nop 0
	global_load_dwordx4 v[2:5], v[2:3], off offset:192
	s_barrier
	global_load_dwordx4 v[18:21], v[18:19], off offset:1024
	s_nop 0
	global_load_dwordx4 v[22:25], v[22:23], off offset:2048
	s_nop 0
	global_load_dwordx4 v[26:29], v[26:27], off offset:1024
	s_nop 0
	global_load_dwordx4 v[30:33], v[30:31], off offset:2048
	s_nop 0
	global_load_dwordx4 v[34:37], v[34:35], off offset:1024
	s_nop 0
	global_load_dwordx4 v[38:41], v[38:39], off offset:2048
	s_nop 0
	global_load_dwordx4 v[42:45], v[42:43], off offset:1024
	s_nop 0
	global_load_dwordx4 v[46:49], v[46:47], off offset:2048
	s_lshr_b32 s52, s50, 8
	s_lshl_b32 s57, s52, 6
	s_cmp_gt_u32 s51, 1
	s_cselect_b64 s[2:3], -1, 0
	s_and_b64 s[6:7], s[2:3], exec
	s_cselect_b32 s33, 16, 0
	s_add_i32 s6, s55, 2
	s_lshl_b32 s7, s6, 6
	s_add_i32 s14, s7, s54
	v_or_b32_e32 v182, s54, v170
	v_or_b32_e32 v179, s54, v106
	v_or_b32_e32 v138, s57, v1
	v_sub_u32_e64 v51, v50, 8 clamp
	v_lshlrev_b32_e32 v54, 2, v50
	v_or_b32_e32 v50, s33, v138
	v_mul_lo_u32 v82, v50, s13
	v_add_u32_e32 v180, v120, v82
	v_min_u32_e32 v62, 48, v51
	v_readlane_b32 s60, v254, 29
	v_readlane_b32 s64, v254, 33
	v_readlane_b32 s65, v254, 34
	s_waitcnt vmcnt(7)
	ds_write_b128 v126, v[18:21]
	s_waitcnt vmcnt(6)
	ds_write_b128 v127, v[22:25] offset:34816
	s_waitcnt vmcnt(5)
	ds_write_b128 v128, v[26:29]
	s_waitcnt vmcnt(4)
	ds_write_b128 v129, v[30:33] offset:34816
	s_waitcnt vmcnt(3)
	ds_write_b128 v126, v[34:37] offset:17408
	s_waitcnt vmcnt(2)
	ds_write_b128 v130, v[38:41] offset:34816
	s_waitcnt vmcnt(1)
	ds_write_b128 v131, v[42:45]
	s_waitcnt vmcnt(0)
	ds_write_b128 v132, v[46:49] offset:34816
	v_or_b32_e32 v18, s14, v168
	v_mul_lo_u32 v86, v18, s46
	v_lshl_add_u64 v[18:19], s[18:19], 0, v[86:87]
	v_add_u32_e32 v26, s7, v182
	v_lshl_add_u64 v[18:19], v[18:19], 0, s[24:25]
	v_mul_lo_u32 v86, v26, s46
	v_lshl_add_u64 v[18:19], v[18:19], 0, v[92:93]
	v_lshl_add_u64 v[26:27], s[18:19], 0, v[86:87]
	v_add_u32_e32 v34, s7, v178
	v_lshl_add_u64 v[20:21], v[18:19], 0, s[10:11]
	v_add_co_u32_e32 v18, vcc, s47, v18
	v_lshl_add_u64 v[26:27], v[26:27], 0, s[24:25]
	v_mul_lo_u32 v86, v34, s46
	v_add_u32_e64 v42, s6, 1
	v_addc_co_u32_e32 v19, vcc, 0, v19, vcc
	v_lshl_add_u64 v[26:27], v[26:27], 0, v[92:93]
	v_lshl_add_u64 v[34:35], s[18:19], 0, v[86:87]
	v_lshl_add_u32 v42, v42, 6, v179
	v_lshl_add_u64 v[28:29], v[26:27], 0, s[10:11]
	v_add_co_u32_e32 v26, vcc, s47, v26
	v_lshl_add_u64 v[34:35], v[34:35], 0, s[24:25]
	v_mul_lo_u32 v86, v42, s46
	v_addc_co_u32_e32 v27, vcc, 0, v27, vcc
	v_lshl_add_u64 v[34:35], v[34:35], 0, v[92:93]
	v_lshl_add_u64 v[42:43], s[18:19], 0, v[86:87]
	v_lshl_add_u64 v[36:37], v[34:35], 0, s[10:11]
	v_add_co_u32_e32 v34, vcc, s47, v34
	v_lshl_add_u64 v[42:43], v[42:43], 0, s[24:25]
	s_nop 0
	v_addc_co_u32_e32 v35, vcc, 0, v35, vcc
	v_lshl_add_u64 v[42:43], v[42:43], 0, v[92:93]
	v_lshl_add_u64 v[44:45], v[42:43], 0, s[10:11]
	v_add_co_u32_e32 v42, vcc, s47, v42
	s_waitcnt lgkmcnt(0)
	s_nop 0
	v_addc_co_u32_e32 v43, vcc, 0, v43, vcc
	s_barrier
; #define LAS __attribute__((address_space(3)))
; __device__ __forceinline__ void na_fast_unit(int unit, const bf16_t* P, const float* rpb, bf16_t* AO, LAS unsigned char* lds) {
;     ...
;         const bool win = s < 4;
;         f32x4 sc[4];
;         const int kr = rstart + 2 * s + kh;
;         const float* bp = rpb + (h * 15 + (win ? kr - r + 7 : 0)) * 31 - col + 15;
; #pragma unroll
;         for (int j = 0; j < 4; ++j) {
;             if (win && j == 3) { sc[j] = (f32x4){-1.0e30f, -1.0e30f, -1.0e30f, -1.0e30f}; }
;             else { const int lk = 64 * kh + (win ? 16 * (ct0 + j) : 16 * j) + l15;
;                 f32x4 X = (f32x4){0.f, 0.f, 0.f, 0.f};
; #pragma unroll
;                 for (int kk = 0; kk < 4; ++kk) { const bf16x8 kf = *(const LAS bf16x8*)(buf + NA_KB + lk * NA_RSK + (32 * kk + 8 * q) * 2); X = __builtin_amdgcn_mfma_f32_16x16x32_bf16(kf, qf[kk], X, 0, 0, 0); }
;                 if (win) {
; #pragma unroll
;                     for (int rg = 0; rg < 4; ++rg) { const int kc = 16 * (ct0 + j) + 4 * q + rg; const bool ok = kc >= cstart && kc < cstart + 16;
;                         float bias = 0.f; if (ok) bias = bp[kc];
;                         sc[j][rg] = ok ? X[rg] * scale + bias : -1.0e30f; }
	s_sub_i32 s80, s55, s16
	s_mul_i32 s81, s56, 15
	s_add_i32 s80, s80, s52
	s_add_i32 s80, s80, s81
	s_add_i32 s80, s80, 7
	s_mul_i32 s80, s80, 31
	v_or_b32_e32 v244, s33, v169
	v_add_u32_e32 v242, s80, v244
	v_lshlrev_b32_e32 v242, 2, v242
	v_sub_u32_e32 v242, v242, v54
	v_ashrrev_i32_e32 v243, 31, v242
	v_sub_u32_e32 v244, v244, v62
	v_lshl_add_u64 v[240:241], v[242:243], 0, s[64:65]
	v_add_u32_e32 v239, 0, v244
	v_cmp_gt_u32_e32 vcc, 16, v239
	s_and_saveexec_b64 s[86:87], vcc
	global_load_dword v226, v[240:241], off offset:60
	s_or_b64 exec, exec, s[86:87]
	v_add_u32_e32 v239, 1, v244
	v_cmp_gt_u32_e32 vcc, 16, v239
	s_and_saveexec_b64 s[86:87], vcc
	global_load_dword v227, v[240:241], off offset:64
	s_or_b64 exec, exec, s[86:87]
	v_add_u32_e32 v239, 2, v244
	v_cmp_gt_u32_e32 vcc, 16, v239
	s_and_saveexec_b64 s[86:87], vcc
	global_load_dword v229, v[240:241], off offset:68
	s_or_b64 exec, exec, s[86:87]
	v_add_u32_e32 v239, 3, v244
	v_cmp_gt_u32_e32 vcc, 16, v239
	s_and_saveexec_b64 s[86:87], vcc
	global_load_dword v230, v[240:241], off offset:72
	s_or_b64 exec, exec, s[86:87]
	v_add_u32_e32 v239, 16, v244
	v_cmp_gt_u32_e32 vcc, 16, v239
	s_and_saveexec_b64 s[86:87], vcc
	global_load_dword v231, v[240:241], off offset:124
	s_or_b64 exec, exec, s[86:87]
	v_add_u32_e32 v239, 17, v244
	v_cmp_gt_u32_e32 vcc, 16, v239
	s_and_saveexec_b64 s[86:87], vcc
	global_load_dword v232, v[240:241], off offset:128
	s_or_b64 exec, exec, s[86:87]
	v_add_u32_e32 v239, 18, v244
	v_cmp_gt_u32_e32 vcc, 16, v239
	s_and_saveexec_b64 s[86:87], vcc
	global_load_dword v233, v[240:241], off offset:132
	s_or_b64 exec, exec, s[86:87]
	v_add_u32_e32 v239, 19, v244
	v_cmp_gt_u32_e32 vcc, 16, v239
	s_and_saveexec_b64 s[86:87], vcc
	global_load_dword v234, v[240:241], off offset:136
	s_or_b64 exec, exec, s[86:87]
	v_add_u32_e32 v239, 32, v244
	v_cmp_gt_u32_e32 vcc, 16, v239
	s_and_saveexec_b64 s[86:87], vcc
	global_load_dword v235, v[240:241], off offset:188
	s_or_b64 exec, exec, s[86:87]
	v_add_u32_e32 v239, 33, v244
	v_cmp_gt_u32_e32 vcc, 16, v239
	s_and_saveexec_b64 s[86:87], vcc
	global_load_dword v236, v[240:241], off offset:192
	s_or_b64 exec, exec, s[86:87]
	v_add_u32_e32 v239, 34, v244
	v_cmp_gt_u32_e32 vcc, 16, v239
	s_and_saveexec_b64 s[86:87], vcc
	global_load_dword v237, v[240:241], off offset:196
	s_or_b64 exec, exec, s[86:87]
	v_add_u32_e32 v239, 35, v244
	v_cmp_gt_u32_e32 vcc, 16, v239
	s_and_saveexec_b64 s[86:87], vcc
	global_load_dword v238, v[240:241], off offset:200
	s_or_b64 exec, exec, s[86:87]
	global_load_dwordx4 v[22:25], v[18:19], off offset:1024
	s_nop 0
	global_load_dwordx4 v[18:21], v[20:21], off offset:2048
	s_nop 0
	global_load_dwordx4 v[30:33], v[26:27], off offset:1024
	s_nop 0
	global_load_dwordx4 v[26:29], v[28:29], off offset:2048
	s_nop 0
	global_load_dwordx4 v[38:41], v[34:35], off offset:1024
	s_nop 0
	global_load_dwordx4 v[34:37], v[36:37], off offset:2048
	s_nop 0
	global_load_dwordx4 v[46:49], v[42:43], off offset:1024
	s_nop 0
	global_load_dwordx4 v[42:45], v[44:45], off offset:2048
	ds_read_b128 v[50:53], v180
	s_mov_b64 s[20:21], s[64:65]
	v_mov_b32_e32 v55, s21
	v_sub_co_u32_e32 v98, vcc, s20, v54
	ds_read_b128 v[58:61], v180 offset:128
	ds_read_b128 v[66:69], v180 offset:192
	v_subbrev_co_u32_e32 v99, vcc, 0, v55, vcc
	ds_read_b128 v[54:57], v180 offset:64
	s_waitcnt lgkmcnt(3)
	v_mfma_f32_16x16x32_bf16 v[50:53], v[50:53], v[14:17], 0
	v_add_u32_e32 v65, 16, v62
	v_or_b32_e32 v94, s33, v169
	v_cmp_ge_u32_e32 vcc, v94, v62
	s_waitcnt lgkmcnt(0)
	v_mfma_f32_16x16x32_bf16 v[50:53], v[54:57], v[10:13], v[50:53]
	v_cmp_lt_u32_e64 s[6:7], v94, v65
	s_and_b64 s[14:15], vcc, s[6:7]
	s_sub_i32 s6, s55, s16
	v_mfma_f32_16x16x32_bf16 v[50:53], v[58:61], v[6:9], v[50:53]
	s_mul_i32 s17, s56, 15
	s_add_i32 s6, s6, s52
	s_add_i32 s6, s6, s17
	s_add_i32 s6, s6, 7
	s_mul_i32 s42, s6, 31
	v_mfma_f32_16x16x32_bf16 v[50:53], v[66:69], v[2:5], v[50:53]
	s_ashr_i32 s43, s42, 31
	v_mov_b32_e32 v95, v87
	v_lshl_add_u64 v[54:55], s[42:43], 2, v[98:99]
	v_mov_b32_e32 v58, 0xf149f2ca
	v_lshl_add_u64 v[56:57], v[94:95], 2, v[54:55]
	v_mov_b32_e32 v59, 0xf149f2ca
	v_readlane_b32 s61, v254, 30
	v_readlane_b32 s62, v254, 31
	v_readlane_b32 s63, v254, 32
	v_readlane_b32 s66, v254, 35
	v_readlane_b32 s67, v254, 36
	v_readlane_b32 s68, v254, 37
	v_readlane_b32 s69, v254, 38
	v_readlane_b32 s70, v254, 39
	v_readlane_b32 s71, v254, 40
	v_readlane_b32 s72, v254, 41
	v_readlane_b32 s73, v254, 42
	v_readlane_b32 s74, v254, 43
	v_readlane_b32 s75, v254, 44
	s_and_saveexec_b64 s[6:7], s[14:15]
	s_cbranch_execz .LBB0_1216
	s_waitcnt vmcnt(8)
	v_mov_b32_e32 v59, v226
	v_fmac_f32_e32 v59, 0x3db504f3, v50
.LBB0_1216:
	s_or_b64 exec, exec, s[6:7]
	v_or_b32_e32 v50, 1, v94
	v_cmp_ge_u32_e32 vcc, v50, v62
	v_cmp_lt_u32_e64 s[6:7], v50, v65
	s_and_b64 s[16:17], vcc, s[6:7]
	s_and_saveexec_b64 s[6:7], s[16:17]
	s_cbranch_execz .LBB0_1218
	s_waitcnt vmcnt(8)
	v_mov_b32_e32 v58, v227
	v_fmac_f32_e32 v58, 0x3db504f3, v51
.LBB0_1218:
	s_or_b64 exec, exec, s[6:7]
	v_or_b32_e32 v50, 2, v94
	v_cmp_ge_u32_e32 vcc, v50, v62
	v_cmp_lt_u32_e64 s[6:7], v50, v65
	s_and_b64 s[18:19], vcc, s[6:7]
	v_mov_b32_e32 v60, 0xf149f2ca
	v_mov_b32_e32 v61, 0xf149f2ca
	s_and_saveexec_b64 s[6:7], s[18:19]
	s_cbranch_execz .LBB0_1220
	s_waitcnt vmcnt(8)
	v_mov_b32_e32 v61, v229
	v_fmac_f32_e32 v61, 0x3db504f3, v52
.LBB0_1220:
	s_or_b64 exec, exec, s[6:7]
	v_or_b32_e32 v50, 3, v94
	v_cmp_ge_u32_e32 vcc, v50, v62
	v_cmp_lt_u32_e64 s[6:7], v50, v65
	s_and_b64 s[20:21], vcc, s[6:7]
	s_and_saveexec_b64 s[6:7], s[20:21]
	s_cbranch_execz .LBB0_1222
	s_waitcnt vmcnt(8)
	v_mov_b32_e32 v60, v230
	v_fmac_f32_e32 v60, 0x3db504f3, v53
; #define LAS __attribute__((address_space(3)))
; __device__ __forceinline__ void na_fast_unit(int unit, const bf16_t* P, const float* rpb, bf16_t* AO, LAS unsigned char* lds) {
;     ...
;         for (int j = 0; j < 4; ++j) {
;             if (win && j == 3) { sc[j] = (f32x4){-1.0e30f, -1.0e30f, -1.0e30f, -1.0e30f}; }
;             else { const int lk = 64 * kh + (win ? 16 * (ct0 + j) : 16 * j) + l15;
;                 f32x4 X = (f32x4){0.f, 0.f, 0.f, 0.f};
; #pragma unroll
;                 for (int kk = 0; kk < 4; ++kk) { const bf16x8 kf = *(const LAS bf16x8*)(buf + NA_KB + lk * NA_RSK + (32 * kk + 8 * q) * 2); X = __builtin_amdgcn_mfma_f32_16x16x32_bf16(kf, qf[kk], X, 0, 0, 0); }
;                 if (win) {
; #pragma unroll
;                     for (int rg = 0; rg < 4; ++rg) { const int kc = 16 * (ct0 + j) + 4 * q + rg; const bool ok = kc >= cstart && kc < cstart + 16;
;                         float bias = 0.f; if (ok) bias = bp[kc];
;                         sc[j][rg] = ok ? X[rg] * scale + bias : -1.0e30f; }
;                 } else sc[j] = X * scale; } }
;         float ms = fmaxf(fmaxf(fmaxf(sc[0][0], sc[0][1]), fmaxf(sc[0][2], sc[0][3])), fmaxf(fmaxf(sc[1][0], sc[1][1]), fmaxf(sc[1][2], sc[1][3])));
;         ms = fmaxf(ms, fmaxf(fmaxf(fmaxf(sc[2][0], sc[2][1]), fmaxf(sc[2][2], sc[2][3])), fmaxf(fmaxf(sc[3][0], sc[3][1]), fmaxf(sc[3][2], sc[3][3]))));
;         ms = fmaxf(ms, __shfl_xor(ms, 16)); ms = fmaxf(ms, __shfl_xor(ms, 32));
.LBB0_1222:
	s_or_b64 exec, exec, s[6:7]
	s_and_b64 s[6:7], s[2:3], exec
	s_cselect_b32 s6, 32, 16
	v_or_b32_e32 v50, s6, v138
	v_mul_lo_u32 v146, v50, s13
	v_add_u32_e32 v183, v120, v146
	ds_read_b128 v[50:53], v183
	ds_read_b128 v[66:69], v183 offset:64
	ds_read_b128 v[70:73], v183 offset:128
	v_or_b32_e32 v86, s6, v169
	v_cmp_ge_u32_e32 vcc, v86, v62
	s_waitcnt lgkmcnt(2)
	v_mfma_f32_16x16x32_bf16 v[50:53], v[50:53], v[14:17], 0
	v_cmp_lt_u32_e64 s[6:7], v86, v65
	s_and_b64 s[26:27], vcc, s[6:7]
	v_mov_b32_e32 v63, 0xf149f2ca
	s_waitcnt lgkmcnt(1)
	v_mfma_f32_16x16x32_bf16 v[50:53], v[66:69], v[10:13], v[50:53]
	ds_read_b128 v[66:69], v183 offset:192
	v_lshl_add_u64 v[56:57], v[86:87], 2, v[54:55]
	v_mov_b32_e32 v64, 0xf149f2ca
	s_waitcnt lgkmcnt(1)
	v_mfma_f32_16x16x32_bf16 v[50:53], v[70:73], v[6:9], v[50:53]
	s_waitcnt lgkmcnt(0)
	v_mfma_f32_16x16x32_bf16 v[50:53], v[66:69], v[2:5], v[50:53]
	s_and_saveexec_b64 s[6:7], s[26:27]
	s_cbranch_execz .LBB0_1224
	s_waitcnt vmcnt(8)
	v_mov_b32_e32 v64, v231
	s_nop 3
	v_fmac_f32_e32 v64, 0x3db504f3, v50
.LBB0_1224:
	s_or_b64 exec, exec, s[6:7]
	s_nop 4
	v_or_b32_e32 v50, 1, v86
	v_cmp_ge_u32_e32 vcc, v50, v62
	v_cmp_lt_u32_e64 s[6:7], v50, v65
	s_and_b64 s[28:29], vcc, s[6:7]
	s_and_saveexec_b64 s[6:7], s[28:29]
	s_cbranch_execz .LBB0_1226
	s_waitcnt vmcnt(8)
	v_mov_b32_e32 v63, v232
	v_fmac_f32_e32 v63, 0x3db504f3, v51
.LBB0_1226:
	s_or_b64 exec, exec, s[6:7]
	v_or_b32_e32 v50, 2, v86
	v_cmp_ge_u32_e32 vcc, v50, v62
	v_cmp_lt_u32_e64 s[6:7], v50, v65
	s_and_b64 s[30:31], vcc, s[6:7]
	v_mov_b32_e32 v66, 0xf149f2ca
	v_mov_b32_e32 v67, 0xf149f2ca
	s_and_saveexec_b64 s[6:7], s[30:31]
	s_cbranch_execz .LBB0_1228
	s_waitcnt vmcnt(8)
	v_mov_b32_e32 v67, v233
	v_fmac_f32_e32 v67, 0x3db504f3, v52
.LBB0_1228:
	s_or_b64 exec, exec, s[6:7]
	v_or_b32_e32 v50, 3, v86
	v_cmp_ge_u32_e32 vcc, v50, v62
	v_cmp_lt_u32_e64 s[6:7], v50, v65
	s_and_b64 s[34:35], vcc, s[6:7]
	s_and_saveexec_b64 s[6:7], s[34:35]
	s_cbranch_execz .LBB0_1230
	s_waitcnt vmcnt(8)
	v_mov_b32_e32 v66, v234
	v_fmac_f32_e32 v66, 0x3db504f3, v53
.LBB0_1230:
	s_or_b64 exec, exec, s[6:7]
	s_and_b64 s[2:3], s[2:3], exec
	s_cselect_b32 s2, 48, 32
	v_or_b32_e32 v50, s2, v138
	v_mul_lo_u32 v147, v50, s13
	v_add_u32_e32 v184, v120, v147
	ds_read_b128 v[50:53], v184
	ds_read_b128 v[68:71], v184 offset:64
	ds_read_b128 v[72:75], v184 offset:128
	v_or_b32_e32 v96, s2, v169
	v_cmp_ge_u32_e32 vcc, v96, v62
	s_waitcnt lgkmcnt(2)
	v_mfma_f32_16x16x32_bf16 v[50:53], v[50:53], v[14:17], 0
	v_cmp_lt_u32_e64 s[6:7], v96, v65
	v_mov_b32_e32 v97, v87
	s_and_b64 s[36:37], vcc, s[6:7]
	s_waitcnt lgkmcnt(1)
	v_mfma_f32_16x16x32_bf16 v[50:53], v[68:71], v[10:13], v[50:53]
	ds_read_b128 v[68:71], v184 offset:192
	v_mov_b32_e32 v56, 0xf149f2ca
	v_lshl_add_u64 v[54:55], v[96:97], 2, v[54:55]
	s_waitcnt lgkmcnt(1)
	v_mfma_f32_16x16x32_bf16 v[50:53], v[72:75], v[6:9], v[50:53]
	v_mov_b32_e32 v57, 0xf149f2ca
	s_waitcnt lgkmcnt(0)
	v_mfma_f32_16x16x32_bf16 v[50:53], v[68:71], v[2:5], v[50:53]
	s_and_saveexec_b64 s[2:3], s[36:37]
	s_cbranch_execz .LBB0_1232
	s_waitcnt vmcnt(8)
	v_mov_b32_e32 v57, v235
	s_nop 3
	v_fmac_f32_e32 v57, 0x3db504f3, v50
.LBB0_1232:
	s_or_b64 exec, exec, s[2:3]
	s_nop 4
	v_or_b32_e32 v50, 1, v96
	v_cmp_ge_u32_e32 vcc, v50, v62
	v_cmp_lt_u32_e64 s[6:7], v50, v65
	s_and_b64 s[38:39], vcc, s[6:7]
	s_and_saveexec_b64 s[2:3], s[38:39]
	s_cbranch_execz .LBB0_1234
	s_waitcnt vmcnt(8)
	v_mov_b32_e32 v56, v236
	v_fmac_f32_e32 v56, 0x3db504f3, v51
.LBB0_1234:
	s_or_b64 exec, exec, s[2:3]
	v_or_b32_e32 v50, 2, v96
	v_cmp_ge_u32_e32 vcc, v50, v62
	v_cmp_lt_u32_e64 s[6:7], v50, v65
	s_and_b64 s[40:41], vcc, s[6:7]
	v_mov_b32_e32 v50, 0xf149f2ca
	v_mov_b32_e32 v51, 0xf149f2ca
	s_and_saveexec_b64 s[2:3], s[40:41]
	s_cbranch_execz .LBB0_1236
	s_waitcnt vmcnt(8)
	v_mov_b32_e32 v51, v237
	v_fmac_f32_e32 v51, 0x3db504f3, v52
.LBB0_1236:
	s_or_b64 exec, exec, s[2:3]
	v_or_b32_e32 v52, 3, v96
	v_cmp_ge_u32_e32 vcc, v52, v62
	v_cmp_lt_u32_e64 s[6:7], v52, v65
	s_and_b64 s[6:7], vcc, s[6:7]
	s_and_saveexec_b64 s[2:3], s[6:7]
	s_cbranch_execz .LBB0_1238
	s_waitcnt vmcnt(8)
	v_mov_b32_e32 v50, v238
	v_fmac_f32_e32 v50, 0x3db504f3, v53
.LBB0_1238:
	s_or_b64 exec, exec, s[2:3]
	v_and_b32_e32 v53, 64, v133
	v_xor_b32_e32 v52, 16, v133
	v_add_u32_e32 v54, 64, v53
	v_cmp_lt_i32_e32 vcc, v52, v54
	v_max_f32_e32 v55, v57, v57
	v_max_f32_e32 v62, v51, v51
	v_cndmask_b32_e32 v52, v133, v52, vcc
	v_lshlrev_b32_e32 v134, 2, v52
	v_xor_b32_e32 v52, 32, v133
	v_cmp_lt_i32_e32 vcc, v52, v54
	v_max_f32_e32 v54, v67, v67
	v_mov_b32_e32 v161, 0xf149f2ca
	v_cndmask_b32_e32 v52, v133, v52, vcc
	v_lshlrev_b32_e32 v91, 2, v52
	v_or_b32_e32 v52, v53, v169
	v_lshlrev_b32_e32 v136, 2, v52
	v_max_f32_e32 v52, v60, v60
	v_max_f32_e32 v53, v61, v61
	v_max_f32_e32 v52, v53, v52
	v_max_f32_e32 v53, v66, v66
	v_max_f32_e32 v53, v54, v53
	v_max_f32_e32 v54, v56, v56
	v_max_f32_e32 v54, v55, v54
	v_max_f32_e32 v55, v50, v50
	v_max_f32_e32 v55, v62, v55
	v_max3_f32 v52, v59, v58, v52
	v_max3_f32 v53, v64, v63, v53
	v_max3_f32 v54, v54, v55, v161
	v_max3_f32 v52, v52, v53, v54
	ds_bpermute_b32 v53, v134, v52
	v_or_b32_e32 v137, s57, v173
	v_or_b32_e32 v135, 12, v136
	s_add_i32 s3, s55, 4
	v_add_u32_e32 v139, v122, v107
	s_waitcnt lgkmcnt(0)
	v_max_f32_e32 v53, v53, v53
	v_max_f32_e32 v52, v52, v53
	ds_bpermute_b32 v53, v91, v52
	s_lshl_b32 s2, s56, 7
	v_readlane_b32 s56, v254, 61
	v_readlane_b32 s57, v254, 62
	v_mov_b32_e32 v93, v87
	s_waitcnt lgkmcnt(0)
; #define NA_STORE(bufp) do { _Pragma("unroll") for (int i_ = 0; i_ < 4; ++i_) { const int id = tid + 512 * i_, key = id >> 4, ch = id & 15; \
;         *(LAS u32x4*)((bufp) + NA_KB + key * NA_RSK + ch * 16) = rk[i_]; *(LAS u32x4*)((bufp) + NA_VB + key * NA_RSV + ch * 16) = rv[i_]; } } while (0)
; __device__ __forceinline__ void na_fast_unit(int unit, const bf16_t* P, const float* rpb, bf16_t* AO, LAS unsigned char* lds) {
;     ...
;         const float mn = fmaxf(m, ms), alpha = __expf(m - mn);
;         m = mn;
;         float ps = 0.f;
; #pragma unroll
;         for (int j = 0; j < 4; ++j)
; #pragma unroll
;             for (int rg = 0; rg < 4; ++rg) { const float p = __expf(sc[j][rg] - mn); sc[j][rg] = p; ps += p; }
;         l = l * alpha + ps;
;         float az[4];
; #pragma unroll
;         for (int rg = 0; rg < 4; ++rg) az[rg] = __shfl(alpha, 4 * q + rg);
; #pragma unroll
;         for (int c = 0; c < 8; ++c)
; #pragma unroll
;             for (int rg = 0; rg < 4; ++rg) accO[c][rg] *= az[rg];
; #pragma unroll
;         for (int pi = 0; pi < 2; ++pi) {
;             const u32x4 pw = (u32x4){pk2(sc[2 * pi][0], sc[2 * pi][1]), pk2(sc[2 * pi][2], sc[2 * pi][3]), pk2(sc[2 * pi + 1][0], sc[2 * pi + 1][1]), pk2(sc[2 * pi + 1][2], sc[2 * pi + 1][3])};
;             const bf16x8 pa = __builtin_bit_cast(bf16x8, pw);
;             const int lk0 = 64 * kh + (win ? 16 * (ct0 + 2 * pi) : 32 * pi) + 4 * q + trq;
;             const int hoff = (win && pi == 1) ? 0 : 16 * NA_RSV;
; #pragma unroll
;             for (int c = 0; c < 8; ++c) { const bf16x8 vf = tr_frag(buf + NA_VB + lk0 * NA_RSV + (16 * c + 4 * trp) * 2, hoff);
;                 accO[c] = __builtin_amdgcn_mfma_f32_16x16x32_bf16(pa, vf, accO[c], 0, 0, 0); }
;         }
;         if (s + 1 < 6) NA_STORE(lds + ((s + 1) & 1) * NA_BUF);
	v_max3_f32 v162, v52, v53, v161
	v_sub_f32_e32 v53, v59, v162
	v_mul_f32_e32 v53, 0x3fb8aa3b, v53
	v_exp_f32_e32 v148, v53
	v_sub_f32_e32 v53, v58, v162
	v_mul_f32_e32 v53, 0x3fb8aa3b, v53
	v_exp_f32_e32 v149, v53
	v_sub_f32_e32 v53, v61, v162
	v_mul_f32_e32 v53, 0x3fb8aa3b, v53
	v_exp_f32_e32 v150, v53
	v_sub_f32_e32 v53, v60, v162
	v_mul_f32_e32 v53, 0x3fb8aa3b, v53
	v_exp_f32_e32 v151, v53
	v_sub_f32_e32 v53, v64, v162
	v_mul_f32_e32 v53, 0x3fb8aa3b, v53
	v_exp_f32_e32 v152, v53
	v_sub_f32_e32 v53, v63, v162
	v_mul_f32_e32 v53, 0x3fb8aa3b, v53
	v_exp_f32_e32 v153, v53
	v_sub_f32_e32 v53, v67, v162
	v_mul_f32_e32 v53, 0x3fb8aa3b, v53
	v_sub_f32_e32 v52, 0xf149f2ca, v162
	v_exp_f32_e32 v154, v53
	v_sub_f32_e32 v53, v66, v162
	v_mul_f32_e32 v52, 0x3fb8aa3b, v52
	v_mul_f32_e32 v53, 0x3fb8aa3b, v53
	v_exp_f32_e32 v155, v53
	v_sub_f32_e32 v53, v57, v162
	v_exp_f32_e32 v160, v52
	v_mul_f32_e32 v53, 0x3fb8aa3b, v53
	v_exp_f32_e32 v156, v53
	v_sub_f32_e32 v53, v56, v162
	v_sub_f32_e32 v51, v51, v162
	v_sub_f32_e32 v50, v50, v162
	v_or_b32_e32 v58, s33, v137
	v_mul_f32_e32 v53, 0x3fb8aa3b, v53
	v_mul_f32_e32 v51, 0x3fb8aa3b, v51
	v_mul_f32_e32 v50, 0x3fb8aa3b, v50
	v_mul_lo_u32 v192, v58, s44
	v_exp_f32_e32 v157, v53
	v_exp_f32_e32 v158, v51
	v_exp_f32_e32 v159, v50
	ds_bpermute_b32 v50, v136, v160
	ds_bpermute_b32 v51, v136, v160 offset:4
	ds_bpermute_b32 v52, v136, v160 offset:8
	ds_bpermute_b32 v53, v135, v160
	v_add_u32_e32 v177, v121, v192
	v_cvt_pk_bf16_f32 v54, v148, v149
	v_cvt_pk_bf16_f32 v55, v150, v151
	v_cvt_pk_bf16_f32 v56, v152, v153
	v_cvt_pk_bf16_f32 v57, v154, v155
	ds_read_b64_tr_b16 v[60:61], v177 offset:39424
	ds_read_b64_tr_b16 v[58:59], v177 offset:34816
	ds_read_b64_tr_b16 v[62:63], v177 offset:34848
	ds_read_b64_tr_b16 v[64:65], v177 offset:39456
	ds_read_b64_tr_b16 v[66:67], v177 offset:34880
	ds_read_b64_tr_b16 v[68:69], v177 offset:39488
	ds_read_b64_tr_b16 v[70:71], v177 offset:34912
	ds_read_b64_tr_b16 v[72:73], v177 offset:39520
	ds_read_b64_tr_b16 v[74:75], v177 offset:34944
	ds_read_b64_tr_b16 v[76:77], v177 offset:39552
	ds_read_b64_tr_b16 v[78:79], v177 offset:34976
	ds_read_b64_tr_b16 v[80:81], v177 offset:39584
	ds_read_b64_tr_b16 v[100:101], v177 offset:35008
	ds_read_b64_tr_b16 v[102:103], v177 offset:39616
	ds_read_b64_tr_b16 v[140:141], v177 offset:35040
	ds_read_b64_tr_b16 v[142:143], v177 offset:39648
	s_waitcnt lgkmcnt(14)
	v_pk_mul_f32 v[52:53], v[52:53], 0 op_sel_hi:[1,0]
	v_pk_mul_f32 v[50:51], v[50:51], 0 op_sel_hi:[1,0]
	v_cvt_pk_bf16_f32 v166, v160, v160
	v_cvt_pk_bf16_f32 v164, v156, v157
	v_mfma_f32_16x16x32_bf16 v[58:61], v[54:57], v[58:61], v[50:53]
	v_cvt_pk_bf16_f32 v165, v158, v159
	v_mov_b32_e32 v167, v166
	v_add_u32_e32 v144, v122, v110
	s_waitcnt lgkmcnt(12)
	v_mfma_f32_16x16x32_bf16 v[62:65], v[54:57], v[62:65], v[50:53]
	v_add_u32_e32 v145, v123, v111
	v_add_u32_e32 v181, v112, v82
	s_waitcnt lgkmcnt(10)
	v_mfma_f32_16x16x32_bf16 v[66:69], v[54:57], v[66:69], v[50:53]
	s_waitcnt lgkmcnt(8)
	v_mfma_f32_16x16x32_bf16 v[70:73], v[54:57], v[70:73], v[50:53]
	s_waitcnt lgkmcnt(6)
	v_mfma_f32_16x16x32_bf16 v[74:77], v[54:57], v[74:77], v[50:53]
	s_waitcnt lgkmcnt(4)
	v_mfma_f32_16x16x32_bf16 v[78:81], v[54:57], v[78:81], v[50:53]
	s_waitcnt lgkmcnt(2)
	v_mfma_f32_16x16x32_bf16 v[100:103], v[54:57], v[100:103], v[50:53]
	s_waitcnt lgkmcnt(0)
	v_mfma_f32_16x16x32_bf16 v[140:143], v[54:57], v[140:143], v[50:53]
	s_nop 2
	v_add_u32_e32 v50, s33, v137
	v_mul_lo_u32 v50, v50, s44
	v_add_u32_e32 v193, 0x2400, v50
	v_add_u32_e32 v176, v121, v193
	ds_read_b64_tr_b16 v[50:51], v176 offset:34816
	ds_read_b64_tr_b16 v[54:55], v176 offset:34848
	s_lshl_b32 s33, s3, 6
	s_add_i32 s24, s33, s54
	s_waitcnt lgkmcnt(1)
	v_mov_b32_e32 v52, v50
	v_mov_b32_e32 v53, v51
	s_waitcnt lgkmcnt(0)
	v_mov_b32_e32 v56, v54
	v_mov_b32_e32 v57, v55
	v_mfma_f32_16x16x32_bf16 v[50:53], v[164:167], v[50:53], v[58:61]
	s_nop 0
	v_mfma_f32_16x16x32_bf16 v[54:57], v[164:167], v[54:57], v[62:65]
	s_nop 0
	ds_read_b64_tr_b16 v[58:59], v176 offset:34880
	s_nop 0
	ds_read_b64_tr_b16 v[62:63], v176 offset:34912
	s_waitcnt lgkmcnt(1)
	v_mov_b32_e32 v60, v58
	v_mov_b32_e32 v61, v59
	s_waitcnt lgkmcnt(0)
	v_mov_b32_e32 v64, v62
	v_mov_b32_e32 v65, v63
	v_mfma_f32_16x16x32_bf16 v[58:61], v[164:167], v[58:61], v[66:69]
	s_nop 0
	v_mfma_f32_16x16x32_bf16 v[62:65], v[164:167], v[62:65], v[70:73]
	s_nop 0
	ds_read_b64_tr_b16 v[66:67], v176 offset:34944
	s_nop 0
	ds_read_b64_tr_b16 v[70:71], v176 offset:34976
	s_waitcnt lgkmcnt(1)
	v_mov_b32_e32 v68, v66
	v_mov_b32_e32 v69, v67
	s_waitcnt lgkmcnt(0)
	v_mov_b32_e32 v72, v70
	v_mov_b32_e32 v73, v71
	v_mfma_f32_16x16x32_bf16 v[66:69], v[164:167], v[66:69], v[74:77]
	s_nop 0
	v_mfma_f32_16x16x32_bf16 v[70:73], v[164:167], v[70:73], v[78:81]
	s_nop 0
	ds_read_b64_tr_b16 v[74:75], v176 offset:35008
	s_nop 0
	ds_read_b64_tr_b16 v[78:79], v176 offset:35040
	s_waitcnt vmcnt(7)
	ds_write_b128 v139, v[22:25]
	s_waitcnt lgkmcnt(2)
	v_mov_b32_e32 v76, v74
	v_mov_b32_e32 v77, v75
	s_waitcnt lgkmcnt(1)
	v_mov_b32_e32 v80, v78
	v_mov_b32_e32 v81, v79
	v_mfma_f32_16x16x32_bf16 v[74:77], v[164:167], v[74:77], v[100:103]
	s_nop 0
	v_mfma_f32_16x16x32_bf16 v[78:81], v[164:167], v[78:81], v[140:143]
	s_nop 2
	v_add_u32_e32 v140, v123, v171
	s_waitcnt vmcnt(6)
	ds_write_b128 v140, v[18:21]
	v_or_b32_e32 v18, s24, v168
	v_add_u32_e32 v141, v122, v108
	v_add_u32_e32 v142, v123, v172
	v_mul_lo_u32 v18, v18, s46
	v_mov_b32_e32 v19, v87
	s_waitcnt vmcnt(5)
	ds_write_b128 v141, v[30:33]
	s_waitcnt vmcnt(4)
	ds_write_b128 v142, v[26:29]
	s_waitcnt vmcnt(3)
; #define LAS __attribute__((address_space(3)))
; __device__ __forceinline__ void na_fast_unit(int unit, const bf16_t* P, const float* rpb, bf16_t* AO, LAS unsigned char* lds) {
;     ...
;         if (s + 1 < 6) NA_LOAD(s + 1);
;         const bool win = s < 4;
;         f32x4 sc[4];
;         const int kr = rstart + 2 * s + kh;
;         const float* bp = rpb + (h * 15 + (win ? kr - r + 7 : 0)) * 31 - col + 15;
; #pragma unroll
;         for (int j = 0; j < 4; ++j) {
;             if (win && j == 3) { sc[j] = (f32x4){-1.0e30f, -1.0e30f, -1.0e30f, -1.0e30f}; }
;             else { const int lk = 64 * kh + (win ? 16 * (ct0 + j) : 16 * j) + l15;
;                 f32x4 X = (f32x4){0.f, 0.f, 0.f, 0.f};
; #pragma unroll
;                 for (int kk = 0; kk < 4; ++kk) { const bf16x8 kf = *(const LAS bf16x8*)(buf + NA_KB + lk * NA_RSK + (32 * kk + 8 * q) * 2); X = __builtin_amdgcn_mfma_f32_16x16x32_bf16(kf, qf[kk], X, 0, 0, 0); }
;                 if (win) {
; #pragma unroll
;                     for (int rg = 0; rg < 4; ++rg) { const int kc = 16 * (ct0 + j) + 4 * q + rg; const bool ok = kc >= cstart && kc < cstart + 16;
;                         float bias = 0.f; if (ok) bias = bp[kc];
;                         sc[j][rg] = ok ? X[rg] * scale + bias : -1.0e30f; }
	ds_write_b128 v139, v[38:41] offset:17408
	v_lshl_add_u64 v[18:19], s[56:57], 0, v[18:19]
	s_lshl_b32 s24, s2, 1
	v_add_u32_e32 v26, s33, v182
	v_add_u32_e32 v143, v123, v109
	v_lshl_add_u64 v[18:19], v[18:19], 0, s[24:25]
	v_mul_lo_u32 v26, v26, s46
	v_mov_b32_e32 v27, v87
	s_waitcnt vmcnt(2)
	ds_write_b128 v143, v[34:37]
	v_lshl_add_u64 v[18:19], v[18:19], 0, v[92:93]
	v_lshl_add_u64 v[26:27], s[56:57], 0, v[26:27]
	v_add_u32_e32 v34, s33, v178
	s_waitcnt vmcnt(1)
	ds_write_b128 v144, v[46:49]
	s_waitcnt vmcnt(0)
	ds_write_b128 v145, v[42:45]
	v_lshl_add_u64 v[22:23], v[18:19], 0, s[10:11]
	v_add_co_u32_e32 v18, vcc, s47, v18
	v_lshl_add_u64 v[26:27], v[26:27], 0, s[24:25]
	v_mul_lo_u32 v34, v34, s46
	v_mov_b32_e32 v35, v87
	v_add_u32_e64 v42, s3, 1
	v_addc_co_u32_e32 v19, vcc, 0, v19, vcc
	v_lshl_add_u64 v[26:27], v[26:27], 0, v[92:93]
	v_lshl_add_u64 v[34:35], s[56:57], 0, v[34:35]
	v_lshl_add_u32 v42, v42, 6, v179
	v_lshl_add_u64 v[30:31], v[26:27], 0, s[10:11]
	v_add_co_u32_e32 v26, vcc, s47, v26
	v_lshl_add_u64 v[34:35], v[34:35], 0, s[24:25]
	v_mul_lo_u32 v42, v42, s46
	v_mov_b32_e32 v43, v87
	v_addc_co_u32_e32 v27, vcc, 0, v27, vcc
	v_lshl_add_u64 v[34:35], v[34:35], 0, v[92:93]
	v_lshl_add_u64 v[42:43], s[56:57], 0, v[42:43]
	v_lshl_add_u64 v[38:39], v[34:35], 0, s[10:11]
	v_add_co_u32_e32 v34, vcc, s47, v34
	v_lshl_add_u64 v[42:43], v[42:43], 0, s[24:25]
	s_nop 0
	v_addc_co_u32_e32 v35, vcc, 0, v35, vcc
	v_lshl_add_u64 v[42:43], v[42:43], 0, v[92:93]
	v_lshl_add_u64 v[46:47], v[42:43], 0, s[10:11]
	v_add_co_u32_e32 v42, vcc, s47, v42
	s_waitcnt lgkmcnt(0)
	s_barrier
	s_nop 0
	v_addc_co_u32_e32 v43, vcc, 0, v43, vcc
	v_add_u32_e32 v239, 0, v244
	v_cmp_gt_u32_e32 vcc, 16, v239
	s_and_saveexec_b64 s[86:87], vcc
	global_load_dword v226, v[240:241], off offset:308
	s_or_b64 exec, exec, s[86:87]
	v_add_u32_e32 v239, 1, v244
	v_cmp_gt_u32_e32 vcc, 16, v239
	s_and_saveexec_b64 s[86:87], vcc
	global_load_dword v227, v[240:241], off offset:312
	s_or_b64 exec, exec, s[86:87]
	v_add_u32_e32 v239, 2, v244
	v_cmp_gt_u32_e32 vcc, 16, v239
	s_and_saveexec_b64 s[86:87], vcc
	global_load_dword v229, v[240:241], off offset:316
	s_or_b64 exec, exec, s[86:87]
	v_add_u32_e32 v239, 3, v244
	v_cmp_gt_u32_e32 vcc, 16, v239
	s_and_saveexec_b64 s[86:87], vcc
	global_load_dword v230, v[240:241], off offset:320
	s_or_b64 exec, exec, s[86:87]
	v_add_u32_e32 v239, 16, v244
	v_cmp_gt_u32_e32 vcc, 16, v239
	s_and_saveexec_b64 s[86:87], vcc
	global_load_dword v231, v[240:241], off offset:372
	s_or_b64 exec, exec, s[86:87]
	v_add_u32_e32 v239, 17, v244
	v_cmp_gt_u32_e32 vcc, 16, v239
	s_and_saveexec_b64 s[86:87], vcc
	global_load_dword v232, v[240:241], off offset:376
	s_or_b64 exec, exec, s[86:87]
	v_add_u32_e32 v239, 18, v244
	v_cmp_gt_u32_e32 vcc, 16, v239
	s_and_saveexec_b64 s[86:87], vcc
	global_load_dword v233, v[240:241], off offset:380
	s_or_b64 exec, exec, s[86:87]
	v_add_u32_e32 v239, 19, v244
	v_cmp_gt_u32_e32 vcc, 16, v239
	s_and_saveexec_b64 s[86:87], vcc
	global_load_dword v234, v[240:241], off offset:384
	s_or_b64 exec, exec, s[86:87]
	v_add_u32_e32 v239, 32, v244
	v_cmp_gt_u32_e32 vcc, 16, v239
	s_and_saveexec_b64 s[86:87], vcc
	global_load_dword v235, v[240:241], off offset:436
	s_or_b64 exec, exec, s[86:87]
	v_add_u32_e32 v239, 33, v244
	v_cmp_gt_u32_e32 vcc, 16, v239
	s_and_saveexec_b64 s[86:87], vcc
	global_load_dword v236, v[240:241], off offset:440
	s_or_b64 exec, exec, s[86:87]
	v_add_u32_e32 v239, 34, v244
	v_cmp_gt_u32_e32 vcc, 16, v239
	s_and_saveexec_b64 s[86:87], vcc
	global_load_dword v237, v[240:241], off offset:444
	s_or_b64 exec, exec, s[86:87]
	v_add_u32_e32 v239, 35, v244
	v_cmp_gt_u32_e32 vcc, 16, v239
	s_and_saveexec_b64 s[86:87], vcc
	global_load_dword v238, v[240:241], off offset:448
	s_or_b64 exec, exec, s[86:87]
	global_load_dwordx4 v[18:21], v[18:19], off offset:1024
	s_nop 0
	global_load_dwordx4 v[22:25], v[22:23], off offset:2048
	s_nop 0
	global_load_dwordx4 v[26:29], v[26:27], off offset:1024
	s_nop 0
	global_load_dwordx4 v[30:33], v[30:31], off offset:2048
	s_nop 0
	global_load_dwordx4 v[34:37], v[34:35], off offset:1024
	s_nop 0
	global_load_dwordx4 v[38:41], v[38:39], off offset:2048
	s_nop 0
	global_load_dwordx4 v[42:45], v[42:43], off offset:1024
	s_nop 0
	global_load_dwordx4 v[46:49], v[46:47], off offset:2048
	ds_read_b128 v[82:85], v181
	ds_read_b128 v[164:167], v181 offset:64
	s_waitcnt lgkmcnt(1)
	v_mfma_f32_16x16x32_bf16 v[82:85], v[82:85], v[14:17], 0
	s_add_i32 s2, s42, 62
	s_ashr_i32 s3, s2, 31
	v_lshl_add_u64 v[100:101], s[2:3], 2, v[98:99]
	s_waitcnt lgkmcnt(0)
	v_mfma_f32_16x16x32_bf16 v[82:85], v[164:167], v[10:13], v[82:85]
	ds_read_b128 v[164:167], v181 offset:128
	v_lshl_add_u64 v[102:103], v[94:95], 2, v[100:101]
	v_mov_b32_e32 v93, 0xf149f2ca
	s_waitcnt lgkmcnt(0)
	v_mfma_f32_16x16x32_bf16 v[82:85], v[164:167], v[6:9], v[82:85]
	ds_read_b128 v[164:167], v181 offset:192
	s_waitcnt lgkmcnt(0)
	v_mfma_f32_16x16x32_bf16 v[82:85], v[164:167], v[2:5], v[82:85]
	s_and_saveexec_b64 s[2:3], s[14:15]
	s_cbranch_execz .LBB0_1240
	s_waitcnt vmcnt(8)
	v_mov_b32_e32 v93, v226
	s_nop 3
	v_fmac_f32_e32 v93, 0x3db504f3, v82
.LBB0_1240:
	s_or_b64 exec, exec, s[2:3]
	s_and_saveexec_b64 s[2:3], s[16:17]
	s_cbranch_execz .LBB0_1242
	s_waitcnt vmcnt(8)
	v_mov_b32_e32 v161, v227
	s_nop 0
	v_fmac_f32_e32 v161, 0x3db504f3, v83
.LBB0_1242:
	s_or_b64 exec, exec, s[2:3]
	v_mov_b32_e32 v163, 0xf149f2ca
	v_mov_b32_e32 v164, 0xf149f2ca
	s_and_saveexec_b64 s[2:3], s[18:19]
	s_cbranch_execz .LBB0_1244
	s_waitcnt vmcnt(8)
	v_mov_b32_e32 v164, v229
	v_fmac_f32_e32 v164, 0x3db504f3, v84
; #define LAS __attribute__((address_space(3)))
; __device__ __forceinline__ void na_fast_unit(int unit, const bf16_t* P, const float* rpb, bf16_t* AO, LAS unsigned char* lds) {
;     ...
;         for (int j = 0; j < 4; ++j) {
;             if (win && j == 3) { sc[j] = (f32x4){-1.0e30f, -1.0e30f, -1.0e30f, -1.0e30f}; }
;             else { const int lk = 64 * kh + (win ? 16 * (ct0 + j) : 16 * j) + l15;
;                 f32x4 X = (f32x4){0.f, 0.f, 0.f, 0.f};
; #pragma unroll
;                 for (int kk = 0; kk < 4; ++kk) { const bf16x8 kf = *(const LAS bf16x8*)(buf + NA_KB + lk * NA_RSK + (32 * kk + 8 * q) * 2); X = __builtin_amdgcn_mfma_f32_16x16x32_bf16(kf, qf[kk], X, 0, 0, 0); }
;                 if (win) {
; #pragma unroll
;                     for (int rg = 0; rg < 4; ++rg) { const int kc = 16 * (ct0 + j) + 4 * q + rg; const bool ok = kc >= cstart && kc < cstart + 16;
;                         float bias = 0.f; if (ok) bias = bp[kc];
;                         sc[j][rg] = ok ? X[rg] * scale + bias : -1.0e30f; }
;                 } else sc[j] = X * scale; } }
;         float ms = fmaxf(fmaxf(fmaxf(sc[0][0], sc[0][1]), fmaxf(sc[0][2], sc[0][3])), fmaxf(fmaxf(sc[1][0], sc[1][1]), fmaxf(sc[1][2], sc[1][3])));
;         ms = fmaxf(ms, fmaxf(fmaxf(fmaxf(sc[2][0], sc[2][1]), fmaxf(sc[2][2], sc[2][3])), fmaxf(fmaxf(sc[3][0], sc[3][1]), fmaxf(sc[3][2], sc[3][3]))));
;         ms = fmaxf(ms, __shfl_xor(ms, 16)); ms = fmaxf(ms, __shfl_xor(ms, 32));
;         const float mn = fmaxf(m, ms), alpha = __expf(m - mn);
;         m = mn;
;         float ps = 0.f;
; #pragma unroll
;         for (int j = 0; j < 4; ++j)
; #pragma unroll
;             for (int rg = 0; rg < 4; ++rg) { const float p = __expf(sc[j][rg] - mn); sc[j][rg] = p; ps += p; }
;         l = l * alpha + ps;
;         float az[4];
; #pragma unroll
;         for (int rg = 0; rg < 4; ++rg) az[rg] = __shfl(alpha, 4 * q + rg);
.LBB0_1244:
	s_or_b64 exec, exec, s[2:3]
	s_and_saveexec_b64 s[2:3], s[20:21]
	s_cbranch_execz .LBB0_1246
	s_waitcnt vmcnt(8)
	v_mov_b32_e32 v163, v230
	v_fmac_f32_e32 v163, 0x3db504f3, v85
.LBB0_1246:
	s_or_b64 exec, exec, s[2:3]
	v_add_u32_e32 v185, v112, v146
	ds_read_b128 v[82:85], v185
	ds_read_b128 v[186:189], v185 offset:64
	v_mov_b32_e32 v165, 0xf149f2ca
	v_lshl_add_u64 v[102:103], v[86:87], 2, v[100:101]
	v_mov_b32_e32 v166, 0xf149f2ca
	s_waitcnt lgkmcnt(1)
	v_mfma_f32_16x16x32_bf16 v[82:85], v[82:85], v[14:17], 0
	s_waitcnt lgkmcnt(0)
	v_mfma_f32_16x16x32_bf16 v[82:85], v[186:189], v[10:13], v[82:85]
	ds_read_b128 v[186:189], v185 offset:128
	s_waitcnt lgkmcnt(0)
	v_mfma_f32_16x16x32_bf16 v[82:85], v[186:189], v[6:9], v[82:85]
	ds_read_b128 v[186:189], v185 offset:192
	s_waitcnt lgkmcnt(0)
	v_mfma_f32_16x16x32_bf16 v[82:85], v[186:189], v[2:5], v[82:85]
	s_and_saveexec_b64 s[2:3], s[26:27]
	s_cbranch_execz .LBB0_1248
	s_waitcnt vmcnt(8)
	v_mov_b32_e32 v166, v231
	s_nop 3
	v_fmac_f32_e32 v166, 0x3db504f3, v82
.LBB0_1248:
	s_or_b64 exec, exec, s[2:3]
	s_and_saveexec_b64 s[2:3], s[28:29]
	s_cbranch_execz .LBB0_1250
	s_waitcnt vmcnt(8)
	v_mov_b32_e32 v165, v232
	s_nop 0
	v_fmac_f32_e32 v165, 0x3db504f3, v83
.LBB0_1250:
	s_or_b64 exec, exec, s[2:3]
	v_mov_b32_e32 v167, 0xf149f2ca
	v_mov_b32_e32 v174, 0xf149f2ca
	s_and_saveexec_b64 s[2:3], s[30:31]
	s_cbranch_execz .LBB0_1252
	s_waitcnt vmcnt(8)
	v_mov_b32_e32 v174, v233
	v_fmac_f32_e32 v174, 0x3db504f3, v84
.LBB0_1252:
	s_or_b64 exec, exec, s[2:3]
	s_and_saveexec_b64 s[2:3], s[34:35]
	s_cbranch_execz .LBB0_1254
	s_waitcnt vmcnt(8)
	v_mov_b32_e32 v167, v234
	v_fmac_f32_e32 v167, 0x3db504f3, v85
.LBB0_1254:
	s_or_b64 exec, exec, s[2:3]
	v_add_u32_e32 v191, v112, v147
	ds_read_b128 v[82:85], v191
	ds_read_b128 v[186:189], v191 offset:64
	v_mov_b32_e32 v102, 0xf149f2ca
	v_lshl_add_u64 v[100:101], v[96:97], 2, v[100:101]
	v_mov_b32_e32 v103, 0xf149f2ca
	s_waitcnt lgkmcnt(1)
	v_mfma_f32_16x16x32_bf16 v[82:85], v[82:85], v[14:17], 0
	s_waitcnt lgkmcnt(0)
	v_mfma_f32_16x16x32_bf16 v[82:85], v[186:189], v[10:13], v[82:85]
	ds_read_b128 v[186:189], v191 offset:128
	s_waitcnt lgkmcnt(0)
	v_mfma_f32_16x16x32_bf16 v[82:85], v[186:189], v[6:9], v[82:85]
	ds_read_b128 v[186:189], v191 offset:192
	s_waitcnt lgkmcnt(0)
	v_mfma_f32_16x16x32_bf16 v[82:85], v[186:189], v[2:5], v[82:85]
	s_and_saveexec_b64 s[2:3], s[36:37]
	s_cbranch_execz .LBB0_1256
	s_waitcnt vmcnt(8)
	v_mov_b32_e32 v103, v235
	s_nop 3
	v_fmac_f32_e32 v103, 0x3db504f3, v82
.LBB0_1256:
	s_or_b64 exec, exec, s[2:3]
	s_and_saveexec_b64 s[2:3], s[38:39]
	s_cbranch_execz .LBB0_1258
	s_waitcnt vmcnt(8)
	v_mov_b32_e32 v102, v236
	s_nop 0
	v_fmac_f32_e32 v102, 0x3db504f3, v83
.LBB0_1258:
	s_or_b64 exec, exec, s[2:3]
	s_nop 1
	v_mov_b32_e32 v82, 0xf149f2ca
	v_mov_b32_e32 v83, 0xf149f2ca
	s_and_saveexec_b64 s[2:3], s[40:41]
	s_cbranch_execz .LBB0_1260
	s_waitcnt vmcnt(8)
	v_mov_b32_e32 v83, v237
	v_fmac_f32_e32 v83, 0x3db504f3, v84
.LBB0_1260:
	s_or_b64 exec, exec, s[2:3]
	s_and_saveexec_b64 s[2:3], s[6:7]
	s_cbranch_execz .LBB0_1262
	s_waitcnt vmcnt(8)
	v_mov_b32_e32 v82, v238
	v_fmac_f32_e32 v82, 0x3db504f3, v85
.LBB0_1262:
	s_or_b64 exec, exec, s[2:3]
	v_max_f32_e32 v84, v163, v163
	v_max_f32_e32 v85, v164, v164
	v_max_f32_e32 v84, v85, v84
	v_max_f32_e32 v85, v167, v167
	v_max_f32_e32 v100, v174, v174
	v_max_f32_e32 v85, v100, v85
	v_max_f32_e32 v100, v102, v102
	v_max_f32_e32 v101, v103, v103
	v_max_f32_e32 v100, v101, v100
	v_max_f32_e32 v101, v82, v82
	v_max_f32_e32 v175, v83, v83
	v_max_f32_e32 v101, v175, v101
	v_mov_b32_e32 v194, 0xf149f2ca
	v_max3_f32 v84, v93, v161, v84
	v_max3_f32 v85, v166, v165, v85
	v_max3_f32 v100, v100, v101, v194
	v_max3_f32 v84, v84, v85, v100
	ds_bpermute_b32 v85, v134, v84
	v_or_b32_e32 v146, 4, v136
	v_or_b32_e32 v147, 8, v136
	v_add_u32_e32 v192, v113, v192
	v_add_u32_e32 v193, v113, v193
	s_waitcnt lgkmcnt(0)
	v_max_f32_e32 v85, v85, v85
	v_max_f32_e32 v84, v84, v85
	ds_bpermute_b32 v85, v91, v84
	s_add_i32 s55, s55, 6
	s_lshl_b32 s2, s55, 6
	s_add_i32 s3, s2, s54
	v_readlane_b32 s56, v254, 61
	s_waitcnt lgkmcnt(0)
	v_max3_f32 v195, v162, v84, v85
	v_sub_f32_e32 v85, v93, v195
	v_mul_f32_e32 v85, 0x3fb8aa3b, v85
	v_exp_f32_e32 v187, v85
	v_sub_f32_e32 v85, v161, v195
	v_mul_f32_e32 v85, 0x3fb8aa3b, v85
	v_exp_f32_e32 v186, v85
	v_sub_f32_e32 v85, v164, v195
	v_mul_f32_e32 v85, 0x3fb8aa3b, v85
	v_exp_f32_e32 v188, v85
	v_sub_f32_e32 v85, v163, v195
	v_mul_f32_e32 v85, 0x3fb8aa3b, v85
	v_exp_f32_e32 v189, v85
	v_sub_f32_e32 v85, v166, v195
	v_mul_f32_e32 v85, 0x3fb8aa3b, v85
	v_exp_f32_e32 v190, v85
	v_sub_f32_e32 v85, v165, v195
	v_mul_f32_e32 v85, 0x3fb8aa3b, v85
	v_sub_f32_e32 v84, v162, v195
	v_exp_f32_e32 v175, v85
	v_sub_f32_e32 v85, v174, v195
	v_mul_f32_e32 v84, 0x3fb8aa3b, v84
	v_mul_f32_e32 v85, 0x3fb8aa3b, v85
	v_exp_f32_e32 v174, v85
	v_sub_f32_e32 v85, v167, v195
	v_exp_f32_e32 v166, v84
	v_mul_f32_e32 v85, 0x3fb8aa3b, v85
	v_exp_f32_e32 v167, v85
	v_sub_f32_e32 v85, v103, v195
	v_mul_f32_e32 v85, 0x3fb8aa3b, v85
	v_exp_f32_e32 v161, v85
	v_sub_f32_e32 v85, v102, v195
	ds_bpermute_b32 v100, v136, v166
	ds_bpermute_b32 v101, v146, v166
	ds_bpermute_b32 v102, v147, v166
	ds_bpermute_b32 v103, v135, v166
	v_sub_f32_e32 v82, v82, v195
	v_mul_f32_e32 v82, 0x3fb8aa3b, v82
	v_sub_f32_e32 v83, v83, v195
	v_exp_f32_e32 v165, v82
	v_sub_f32_e32 v82, 0xf149f2ca, v195
	v_mul_f32_e32 v85, 0x3fb8aa3b, v85
	v_mul_f32_e32 v83, 0x3fb8aa3b, v83
	v_mul_f32_e32 v82, 0x3fb8aa3b, v82
	v_exp_f32_e32 v162, v85
	v_exp_f32_e32 v164, v83
	v_exp_f32_e32 v163, v82
	s_waitcnt lgkmcnt(0)
; __device__ __forceinline__ void lds_barrier() { asm volatile("s_waitcnt lgkmcnt(0)" ::: "memory"); __builtin_amdgcn_s_barrier(); asm volatile("" ::: "memory"); }
; #define NA_STORE(bufp) do { _Pragma("unroll") for (int i_ = 0; i_ < 4; ++i_) { const int id = tid + 512 * i_, key = id >> 4, ch = id & 15; \
;         *(LAS u32x4*)((bufp) + NA_KB + key * NA_RSK + ch * 16) = rk[i_]; *(LAS u32x4*)((bufp) + NA_VB + key * NA_RSV + ch * 16) = rv[i_]; } } while (0)
; __device__ __forceinline__ void na_fast_unit(int unit, const bf16_t* P, const float* rpb, bf16_t* AO, LAS unsigned char* lds) {
;     ...
; #pragma unroll
;         for (int c = 0; c < 8; ++c)
; #pragma unroll
;             for (int rg = 0; rg < 4; ++rg) accO[c][rg] *= az[rg];
; #pragma unroll
;         for (int pi = 0; pi < 2; ++pi) {
;             const u32x4 pw = (u32x4){pk2(sc[2 * pi][0], sc[2 * pi][1]), pk2(sc[2 * pi][2], sc[2 * pi][3]), pk2(sc[2 * pi + 1][0], sc[2 * pi + 1][1]), pk2(sc[2 * pi + 1][2], sc[2 * pi + 1][3])};
;             const bf16x8 pa = __builtin_bit_cast(bf16x8, pw);
;             const int lk0 = 64 * kh + (win ? 16 * (ct0 + 2 * pi) : 32 * pi) + 4 * q + trq;
;             const int hoff = (win && pi == 1) ? 0 : 16 * NA_RSV;
; #pragma unroll
;             for (int c = 0; c < 8; ++c) { const bf16x8 vf = tr_frag(buf + NA_VB + lk0 * NA_RSV + (16 * c + 4 * trp) * 2, hoff);
;                 accO[c] = __builtin_amdgcn_mfma_f32_16x16x32_bf16(pa, vf, accO[c], 0, 0, 0); }
;         }
;         if (s + 1 < 6) NA_STORE(lds + ((s + 1) & 1) * NA_BUF);
;         lds_barrier();
	v_pk_mul_f32 v[84:85], v[52:53], v[102:103]
	v_pk_mul_f32 v[82:83], v[50:51], v[100:101]
	v_pk_mul_f32 v[52:53], v[80:81], v[102:103]
	v_pk_mul_f32 v[50:51], v[78:79], v[100:101]
	v_cvt_pk_bf16_f32 v78, v187, v186
	v_cvt_pk_bf16_f32 v79, v188, v189
	v_cvt_pk_bf16_f32 v80, v190, v175
	v_cvt_pk_bf16_f32 v81, v174, v167
	v_pk_mul_f32 v[56:57], v[56:57], v[102:103]
	v_pk_mul_f32 v[54:55], v[54:55], v[100:101]
	v_pk_mul_f32 v[60:61], v[60:61], v[102:103]
	v_pk_mul_f32 v[58:59], v[58:59], v[100:101]
	v_pk_mul_f32 v[64:65], v[64:65], v[102:103]
	v_pk_mul_f32 v[62:63], v[62:63], v[100:101]
	v_pk_mul_f32 v[68:69], v[68:69], v[102:103]
	v_pk_mul_f32 v[66:67], v[66:67], v[100:101]
	v_pk_mul_f32 v[72:73], v[72:73], v[102:103]
	v_pk_mul_f32 v[70:71], v[70:71], v[100:101]
	v_pk_mul_f32 v[76:77], v[76:77], v[102:103]
	v_pk_mul_f32 v[74:75], v[74:75], v[100:101]
	ds_read_b64_tr_b16 v[102:103], v192 offset:4608
	ds_read_b64_tr_b16 v[100:101], v192
	ds_read_b64_tr_b16 v[196:197], v192 offset:32
	s_waitcnt lgkmcnt(1)
	v_mfma_f32_16x16x32_bf16 v[82:85], v[78:81], v[100:103], v[82:85]
	ds_read_b64_tr_b16 v[198:199], v192 offset:4640
	ds_read_b64_tr_b16 v[100:101], v192 offset:64
	ds_read_b64_tr_b16 v[102:103], v192 offset:4672
	v_readlane_b32 s57, v254, 62
	s_waitcnt lgkmcnt(0)
	v_mfma_f32_16x16x32_bf16 v[58:61], v[78:81], v[100:103], v[58:61]
	ds_read_b64_tr_b16 v[100:101], v192 offset:96
	ds_read_b64_tr_b16 v[102:103], v192 offset:4704
	v_mov_b32_e32 v93, v87
	s_waitcnt lgkmcnt(0)
	v_mfma_f32_16x16x32_bf16 v[62:65], v[78:81], v[100:103], v[62:65]
	ds_read_b64_tr_b16 v[100:101], v192 offset:128
	ds_read_b64_tr_b16 v[102:103], v192 offset:4736
	s_waitcnt lgkmcnt(0)
	v_mfma_f32_16x16x32_bf16 v[66:69], v[78:81], v[100:103], v[66:69]
	ds_read_b64_tr_b16 v[100:101], v192 offset:160
	ds_read_b64_tr_b16 v[102:103], v192 offset:4768
	s_waitcnt lgkmcnt(0)
	v_mfma_f32_16x16x32_bf16 v[70:73], v[78:81], v[100:103], v[70:73]
	ds_read_b64_tr_b16 v[100:101], v192 offset:192
	ds_read_b64_tr_b16 v[102:103], v192 offset:4800
	s_waitcnt lgkmcnt(0)
	v_mfma_f32_16x16x32_bf16 v[74:77], v[78:81], v[100:103], v[74:77]
	ds_read_b64_tr_b16 v[100:101], v192 offset:224
	ds_read_b64_tr_b16 v[102:103], v192 offset:4832
	v_mfma_f32_16x16x32_bf16 v[54:57], v[78:81], v[196:199], v[54:57]
	s_waitcnt lgkmcnt(0)
	v_mfma_f32_16x16x32_bf16 v[78:81], v[78:81], v[100:103], v[50:53]
	v_cvt_pk_bf16_f32 v102, v163, v163
	v_cvt_pk_bf16_f32 v100, v161, v162
	v_cvt_pk_bf16_f32 v101, v164, v165
	v_mov_b32_e32 v103, v102
	ds_read_b64_tr_b16 v[50:51], v193
	ds_read_b64_tr_b16 v[196:197], v193 offset:32
	s_waitcnt lgkmcnt(1)
	v_mov_b32_e32 v52, v50
	v_mov_b32_e32 v53, v51
	s_waitcnt lgkmcnt(0)
	v_mov_b32_e32 v198, v196
	v_mov_b32_e32 v199, v197
	v_mfma_f32_16x16x32_bf16 v[50:53], v[100:103], v[50:53], v[82:85]
	s_nop 2
	ds_read_b64_tr_b16 v[82:83], v193 offset:64
	v_mfma_f32_16x16x32_bf16 v[54:57], v[100:103], v[196:199], v[54:57]
	s_waitcnt lgkmcnt(0)
	v_mov_b32_e32 v84, v82
	v_mov_b32_e32 v85, v83
	s_nop 1
	v_mfma_f32_16x16x32_bf16 v[58:61], v[100:103], v[82:85], v[58:61]
	ds_read_b64_tr_b16 v[82:83], v193 offset:96
	s_waitcnt lgkmcnt(0)
	v_mov_b32_e32 v84, v82
	v_mov_b32_e32 v85, v83
	s_nop 1
	v_mfma_f32_16x16x32_bf16 v[62:65], v[100:103], v[82:85], v[62:65]
	ds_read_b64_tr_b16 v[82:83], v193 offset:128
	s_waitcnt lgkmcnt(0)
	v_mov_b32_e32 v84, v82
	v_mov_b32_e32 v85, v83
	s_nop 1
	v_mfma_f32_16x16x32_bf16 v[66:69], v[100:103], v[82:85], v[66:69]
	ds_read_b64_tr_b16 v[82:83], v193 offset:160
	s_waitcnt lgkmcnt(0)
	v_mov_b32_e32 v84, v82
	v_mov_b32_e32 v85, v83
	s_nop 1
	v_mfma_f32_16x16x32_bf16 v[70:73], v[100:103], v[82:85], v[70:73]
	ds_read_b64_tr_b16 v[82:83], v193 offset:192
	s_waitcnt lgkmcnt(0)
	v_mov_b32_e32 v84, v82
	v_mov_b32_e32 v85, v83
	s_nop 1
	v_mfma_f32_16x16x32_bf16 v[74:77], v[100:103], v[82:85], v[74:77]
	ds_read_b64_tr_b16 v[82:83], v193 offset:224
	s_waitcnt vmcnt(7)
	ds_write_b128 v126, v[18:21]
	s_waitcnt vmcnt(6)
	ds_write_b128 v127, v[22:25] offset:34816
	s_waitcnt vmcnt(5)
	ds_write_b128 v128, v[26:29]
	s_waitcnt vmcnt(4)
	ds_write_b128 v129, v[30:33] offset:34816
	s_waitcnt vmcnt(3)
	ds_write_b128 v126, v[34:37] offset:17408
	s_waitcnt vmcnt(2)
	ds_write_b128 v130, v[38:41] offset:34816
	s_waitcnt vmcnt(1)
	ds_write_b128 v131, v[42:45]
	s_waitcnt vmcnt(0)
	ds_write_b128 v132, v[46:49] offset:34816
	v_or_b32_e32 v18, s3, v168
	v_mul_lo_u32 v18, v18, s46
	v_mov_b32_e32 v19, v87
	v_lshl_add_u64 v[18:19], s[56:57], 0, v[18:19]
	v_add_u32_e32 v26, s2, v182
	v_lshl_add_u64 v[18:19], v[18:19], 0, s[24:25]
	v_mul_lo_u32 v26, v26, s46
	v_mov_b32_e32 v27, v87
	v_lshl_add_u64 v[18:19], v[18:19], 0, v[92:93]
	v_lshl_add_u64 v[26:27], s[56:57], 0, v[26:27]
	v_add_u32_e32 v34, s2, v178
	v_lshl_add_u64 v[22:23], v[18:19], 0, s[10:11]
	v_add_co_u32_e32 v18, vcc, s47, v18
	v_lshl_add_u64 v[26:27], v[26:27], 0, s[24:25]
	v_mul_lo_u32 v34, v34, s46
	v_mov_b32_e32 v35, v87
	v_add_u32_e64 v42, s55, 1
	v_addc_co_u32_e32 v19, vcc, 0, v19, vcc
	v_lshl_add_u64 v[26:27], v[26:27], 0, v[92:93]
	v_lshl_add_u64 v[34:35], s[56:57], 0, v[34:35]
	v_lshl_add_u32 v42, v42, 6, v179
	v_lshl_add_u64 v[30:31], v[26:27], 0, s[10:11]
	v_add_co_u32_e32 v26, vcc, s47, v26
	v_lshl_add_u64 v[34:35], v[34:35], 0, s[24:25]
	v_mul_lo_u32 v42, v42, s46
	v_mov_b32_e32 v43, v87
	v_addc_co_u32_e32 v27, vcc, 0, v27, vcc
	v_lshl_add_u64 v[34:35], v[34:35], 0, v[92:93]
	v_lshl_add_u64 v[42:43], s[56:57], 0, v[42:43]
	v_lshl_add_u64 v[38:39], v[34:35], 0, s[10:11]
	v_add_co_u32_e32 v34, vcc, s47, v34
	v_lshl_add_u64 v[42:43], v[42:43], 0, s[24:25]
	s_nop 0
	v_addc_co_u32_e32 v35, vcc, 0, v35, vcc
	v_lshl_add_u64 v[42:43], v[42:43], 0, v[92:93]
	v_lshl_add_u64 v[46:47], v[42:43], 0, s[10:11]
	v_add_co_u32_e32 v42, vcc, s47, v42
	s_waitcnt lgkmcnt(0)
	s_barrier
; #define LAS __attribute__((address_space(3)))
; __device__ __forceinline__ void na_fast_unit(int unit, const bf16_t* P, const float* rpb, bf16_t* AO, LAS unsigned char* lds) {
;     ...
;     for (int s = 0; s < 6; ++s) {
;         LAS unsigned char* buf = lds + (s & 1) * NA_BUF;
;         if (s + 1 < 6) NA_LOAD(s + 1);
;         const bool win = s < 4;
;         f32x4 sc[4];
;         const int kr = rstart + 2 * s + kh;
;         const float* bp = rpb + (h * 15 + (win ? kr - r + 7 : 0)) * 31 - col + 15;
; #pragma unroll
;         for (int j = 0; j < 4; ++j) {
;             if (win && j == 3) { sc[j] = (f32x4){-1.0e30f, -1.0e30f, -1.0e30f, -1.0e30f}; }
;             else { const int lk = 64 * kh + (win ? 16 * (ct0 + j) : 16 * j) + l15;
;                 f32x4 X = (f32x4){0.f, 0.f, 0.f, 0.f};
; #pragma unroll
;                 for (int kk = 0; kk < 4; ++kk) { const bf16x8 kf = *(const LAS bf16x8*)(buf + NA_KB + lk * NA_RSK + (32 * kk + 8 * q) * 2); X = __builtin_amdgcn_mfma_f32_16x16x32_bf16(kf, qf[kk], X, 0, 0, 0); }
;                 if (win) {
; #pragma unroll
;                     for (int rg = 0; rg < 4; ++rg) { const int kc = 16 * (ct0 + j) + 4 * q + rg; const bool ok = kc >= cstart && kc < cstart + 16;
;                         float bias = 0.f; if (ok) bias = bp[kc];
;                         sc[j][rg] = ok ? X[rg] * scale + bias : -1.0e30f; }
	s_nop 0
	v_addc_co_u32_e32 v43, vcc, 0, v43, vcc
	v_add_u32_e32 v239, 0, v244
	v_cmp_gt_u32_e32 vcc, 16, v239
	s_and_saveexec_b64 s[86:87], vcc
	global_load_dword v226, v[240:241], off offset:556
	s_or_b64 exec, exec, s[86:87]
	v_add_u32_e32 v239, 1, v244
	v_cmp_gt_u32_e32 vcc, 16, v239
	s_and_saveexec_b64 s[86:87], vcc
	global_load_dword v227, v[240:241], off offset:560
	s_or_b64 exec, exec, s[86:87]
	v_add_u32_e32 v239, 2, v244
	v_cmp_gt_u32_e32 vcc, 16, v239
	s_and_saveexec_b64 s[86:87], vcc
	global_load_dword v229, v[240:241], off offset:564
	s_or_b64 exec, exec, s[86:87]
	v_add_u32_e32 v239, 3, v244
	v_cmp_gt_u32_e32 vcc, 16, v239
	s_and_saveexec_b64 s[86:87], vcc
	global_load_dword v230, v[240:241], off offset:568
	s_or_b64 exec, exec, s[86:87]
	v_add_u32_e32 v239, 16, v244
	v_cmp_gt_u32_e32 vcc, 16, v239
	s_and_saveexec_b64 s[86:87], vcc
	global_load_dword v231, v[240:241], off offset:620
	s_or_b64 exec, exec, s[86:87]
	v_add_u32_e32 v239, 17, v244
	v_cmp_gt_u32_e32 vcc, 16, v239
	s_and_saveexec_b64 s[86:87], vcc
	global_load_dword v232, v[240:241], off offset:624
	s_or_b64 exec, exec, s[86:87]
	v_add_u32_e32 v239, 18, v244
	v_cmp_gt_u32_e32 vcc, 16, v239
	s_and_saveexec_b64 s[86:87], vcc
	global_load_dword v233, v[240:241], off offset:628
	s_or_b64 exec, exec, s[86:87]
	v_add_u32_e32 v239, 19, v244
	v_cmp_gt_u32_e32 vcc, 16, v239
	s_and_saveexec_b64 s[86:87], vcc
	global_load_dword v234, v[240:241], off offset:632
	s_or_b64 exec, exec, s[86:87]
	v_add_u32_e32 v239, 32, v244
	v_cmp_gt_u32_e32 vcc, 16, v239
	s_and_saveexec_b64 s[86:87], vcc
	global_load_dword v235, v[240:241], off offset:684
	s_or_b64 exec, exec, s[86:87]
	v_add_u32_e32 v239, 33, v244
	v_cmp_gt_u32_e32 vcc, 16, v239
	s_and_saveexec_b64 s[86:87], vcc
	global_load_dword v236, v[240:241], off offset:688
	s_or_b64 exec, exec, s[86:87]
	v_add_u32_e32 v239, 34, v244
	v_cmp_gt_u32_e32 vcc, 16, v239
	s_and_saveexec_b64 s[86:87], vcc
	global_load_dword v237, v[240:241], off offset:692
	s_or_b64 exec, exec, s[86:87]
	v_add_u32_e32 v239, 35, v244
	v_cmp_gt_u32_e32 vcc, 16, v239
	s_and_saveexec_b64 s[86:87], vcc
	global_load_dword v238, v[240:241], off offset:696
	s_or_b64 exec, exec, s[86:87]
	global_load_dwordx4 v[18:21], v[18:19], off offset:1024
	s_nop 0
	global_load_dwordx4 v[22:25], v[22:23], off offset:2048
	s_nop 0
	global_load_dwordx4 v[26:29], v[26:27], off offset:1024
	s_nop 0
	global_load_dwordx4 v[30:33], v[30:31], off offset:2048
	s_nop 0
	global_load_dwordx4 v[34:37], v[34:35], off offset:1024
	s_nop 0
	global_load_dwordx4 v[38:41], v[38:39], off offset:2048
	s_nop 0
	global_load_dwordx4 v[42:45], v[42:43], off offset:1024
	s_nop 0
	global_load_dwordx4 v[46:49], v[46:47], off offset:2048
	s_waitcnt lgkmcnt(8)
	v_mov_b32_e32 v84, v82
	v_mov_b32_e32 v85, v83
	ds_read_b128 v[196:199], v180 offset:64
	s_add_i32 s2, s42, 0x7c
	v_mfma_f32_16x16x32_bf16 v[78:81], v[100:103], v[82:85], v[78:81]
	ds_read_b128 v[82:85], v180
	s_ashr_i32 s3, s2, 31
	v_lshl_add_u64 v[100:101], s[2:3], 2, v[98:99]
	s_waitcnt lgkmcnt(0)
	v_mfma_f32_16x16x32_bf16 v[82:85], v[82:85], v[14:17], 0
	v_lshl_add_u64 v[102:103], v[94:95], 2, v[100:101]
	v_mov_b32_e32 v93, 0xf149f2ca
	v_mfma_f32_16x16x32_bf16 v[82:85], v[196:199], v[10:13], v[82:85]
	ds_read_b128 v[196:199], v180 offset:128
	s_waitcnt lgkmcnt(0)
	v_mfma_f32_16x16x32_bf16 v[82:85], v[196:199], v[6:9], v[82:85]
	ds_read_b128 v[196:199], v180 offset:192
	s_waitcnt lgkmcnt(0)
	v_mfma_f32_16x16x32_bf16 v[82:85], v[196:199], v[2:5], v[82:85]
	s_and_saveexec_b64 s[2:3], s[14:15]
	s_cbranch_execz .LBB0_1264
	s_waitcnt vmcnt(8)
	v_mov_b32_e32 v93, v226
	s_nop 3
	v_fmac_f32_e32 v93, 0x3db504f3, v82
.LBB0_1264:
	s_or_b64 exec, exec, s[2:3]
	s_and_saveexec_b64 s[2:3], s[16:17]
	s_cbranch_execz .LBB0_1266
	s_waitcnt vmcnt(8)
	v_mov_b32_e32 v194, v227
	s_nop 0
	v_fmac_f32_e32 v194, 0x3db504f3, v83
.LBB0_1266:
	s_or_b64 exec, exec, s[2:3]
	v_mov_b32_e32 v178, 0xf149f2ca
	v_mov_b32_e32 v180, 0xf149f2ca
	s_and_saveexec_b64 s[2:3], s[18:19]
	s_cbranch_execz .LBB0_1268
	s_waitcnt vmcnt(8)
	v_mov_b32_e32 v180, v229
	v_fmac_f32_e32 v180, 0x3db504f3, v84
.LBB0_1268:
	s_or_b64 exec, exec, s[2:3]
	s_and_saveexec_b64 s[2:3], s[20:21]
	s_cbranch_execz .LBB0_1270
	s_waitcnt vmcnt(8)
	v_mov_b32_e32 v178, v230
	v_fmac_f32_e32 v178, 0x3db504f3, v85
.LBB0_1270:
	s_or_b64 exec, exec, s[2:3]
	ds_read_b128 v[82:85], v183
	ds_read_b128 v[196:199], v183 offset:64
	v_mov_b32_e32 v182, 0xf149f2ca
	v_lshl_add_u64 v[102:103], v[86:87], 2, v[100:101]
	s_waitcnt lgkmcnt(1)
	v_mfma_f32_16x16x32_bf16 v[82:85], v[82:85], v[14:17], 0
	s_waitcnt lgkmcnt(0)
	v_mfma_f32_16x16x32_bf16 v[82:85], v[196:199], v[10:13], v[82:85]
	ds_read_b128 v[196:199], v183 offset:128
	s_waitcnt lgkmcnt(0)
	v_mfma_f32_16x16x32_bf16 v[82:85], v[196:199], v[6:9], v[82:85]
	ds_read_b128 v[196:199], v183 offset:192
	s_waitcnt lgkmcnt(0)
	v_mfma_f32_16x16x32_bf16 v[82:85], v[196:199], v[2:5], v[82:85]
	v_mov_b32_e32 v196, 0xf149f2ca
	s_and_saveexec_b64 s[2:3], s[26:27]
	s_cbranch_execz .LBB0_1272
	s_waitcnt vmcnt(8)
	v_mov_b32_e32 v196, v231
	s_nop 2
	v_fmac_f32_e32 v196, 0x3db504f3, v82
.LBB0_1272:
	s_or_b64 exec, exec, s[2:3]
	s_and_saveexec_b64 s[2:3], s[28:29]
	s_cbranch_execz .LBB0_1274
	s_waitcnt vmcnt(8)
	v_mov_b32_e32 v182, v232
	v_fmac_f32_e32 v182, 0x3db504f3, v83
.LBB0_1274:
	s_or_b64 exec, exec, s[2:3]
	v_mov_b32_e32 v197, 0xf149f2ca
	v_mov_b32_e32 v200, 0xf149f2ca
	s_and_saveexec_b64 s[2:3], s[30:31]
	s_cbranch_execz .LBB0_1276
	s_waitcnt vmcnt(8)
	v_mov_b32_e32 v200, v233
	v_fmac_f32_e32 v200, 0x3db504f3, v84
.LBB0_1276:
	s_or_b64 exec, exec, s[2:3]
	s_and_saveexec_b64 s[2:3], s[34:35]
	s_cbranch_execz .LBB0_1278
	s_waitcnt vmcnt(8)
	v_mov_b32_e32 v197, v234
	v_fmac_f32_e32 v197, 0x3db504f3, v85
.LBB0_1278:
	s_or_b64 exec, exec, s[2:3]
	ds_read_b128 v[82:85], v184
	ds_read_b128 v[202:205], v184 offset:64
	v_mov_b32_e32 v201, 0xf149f2ca
	v_lshl_add_u64 v[100:101], v[96:97], 2, v[100:101]
	v_mov_b32_e32 v102, 0xf149f2ca
	s_waitcnt lgkmcnt(1)
	v_mfma_f32_16x16x32_bf16 v[82:85], v[82:85], v[14:17], 0
	s_waitcnt lgkmcnt(0)
	v_mfma_f32_16x16x32_bf16 v[82:85], v[202:205], v[10:13], v[82:85]
	ds_read_b128 v[202:205], v184 offset:128
	s_waitcnt lgkmcnt(0)
	v_mfma_f32_16x16x32_bf16 v[82:85], v[202:205], v[6:9], v[82:85]
	ds_read_b128 v[202:205], v184 offset:192
	s_waitcnt lgkmcnt(0)
	v_mfma_f32_16x16x32_bf16 v[82:85], v[202:205], v[2:5], v[82:85]
	s_and_saveexec_b64 s[2:3], s[36:37]
	s_cbranch_execz .LBB0_1280
	s_waitcnt vmcnt(8)
	v_mov_b32_e32 v102, v235
	s_nop 3
	v_fmac_f32_e32 v102, 0x3db504f3, v82
.LBB0_1280:
	s_or_b64 exec, exec, s[2:3]
	s_and_saveexec_b64 s[2:3], s[38:39]
	s_cbranch_execz .LBB0_1282
	s_waitcnt vmcnt(8)
	v_mov_b32_e32 v201, v236
	s_nop 0
	v_fmac_f32_e32 v201, 0x3db504f3, v83

; __device__ __forceinline__ void na_fast_unit(int unit, const bf16_t* P, const float* rpb, bf16_t* AO, LAS unsigned char* lds) {
;     ...
;         float ms = fmaxf(fmaxf(fmaxf(sc[0][0], sc[0][1]), fmaxf(sc[0][2], sc[0][3])), fmaxf(fmaxf(sc[1][0], sc[1][1]), fmaxf(sc[1][2], sc[1][3])));
;         ms = fmaxf(ms, fmaxf(fmaxf(fmaxf(sc[2][0], sc[2][1]), fmaxf(sc[2][2], sc[2][3])), fmaxf(fmaxf(sc[3][0], sc[3][1]), fmaxf(sc[3][2], sc[3][3]))));
;         ms = fmaxf(ms, __shfl_xor(ms, 16)); ms = fmaxf(ms, __shfl_xor(ms, 32));
;         const float mn = fmaxf(m, ms), alpha = __expf(m - mn);
;         m = mn;
;         float ps = 0.f;
; #pragma unroll
;         for (int j = 0; j < 4; ++j)
; #pragma unroll
;             for (int rg = 0; rg < 4; ++rg) { const float p = __expf(sc[j][rg] - mn); sc[j][rg] = p; ps += p; }
;         l = l * alpha + ps;
;         float az[4];
; #pragma unroll
;         for (int rg = 0; rg < 4; ++rg) az[rg] = __shfl(alpha, 4 * q + rg);
; #pragma unroll
;         for (int c = 0; c < 8; ++c)
; #pragma unroll
;             for (int rg = 0; rg < 4; ++rg) accO[c][rg] *= az[rg];
; #pragma unroll
;         for (int pi = 0; pi < 2; ++pi) {
;             const u32x4 pw = (u32x4){pk2(sc[2 * pi][0], sc[2 * pi][1]), pk2(sc[2 * pi][2], sc[2 * pi][3]), pk2(sc[2 * pi + 1][0], sc[2 * pi + 1][1]), pk2(sc[2 * pi + 1][2], sc[2 * pi + 1][3])};
;             const bf16x8 pa = __builtin_bit_cast(bf16x8, pw);
;             const int lk0 = 64 * kh + (win ? 16 * (ct0 + 2 * pi) : 32 * pi) + 4 * q + trq;
;             const int hoff = (win && pi == 1) ? 0 : 16 * NA_RSV;
; #pragma unroll
;             for (int c = 0; c < 8; ++c) { const bf16x8 vf = tr_frag(buf + NA_VB + lk0 * NA_RSV + (16 * c + 4 * trp) * 2, hoff);
;                 accO[c] = __builtin_amdgcn_mfma_f32_16x16x32_bf16(pa, vf, accO[c], 0, 0, 0); }
.LBB0_1286:
	s_or_b64 exec, exec, s[2:3]
	v_max_f32_e32 v84, v178, v178
	v_max_f32_e32 v85, v180, v180
	v_max_f32_e32 v84, v85, v84
	v_max_f32_e32 v85, v197, v197
	v_max_f32_e32 v100, v200, v200
	v_max_f32_e32 v85, v100, v85
	v_max_f32_e32 v100, v201, v201
	v_max_f32_e32 v101, v102, v102
	v_max_f32_e32 v100, v101, v100
	v_max_f32_e32 v101, v82, v82
	v_max_f32_e32 v103, v83, v83
	v_max_f32_e32 v101, v103, v101
	v_mov_b32_e32 v198, 0xf149f2ca
	v_max3_f32 v84, v93, v194, v84
	v_max3_f32 v85, v196, v182, v85
	v_max3_f32 v100, v100, v101, v198
	v_max3_f32 v84, v84, v85, v100
	ds_bpermute_b32 v85, v134, v84
	s_lshl_b32 s43, s53, 8
	s_or_b32 s2, s43, 0x4000
	v_readlane_b32 s54, v254, 61
	v_readlane_b32 s55, v254, 62
	s_waitcnt lgkmcnt(0)
	v_max_f32_e32 v85, v85, v85
	v_max_f32_e32 v84, v84, v85
	ds_bpermute_b32 v85, v91, v84
	s_waitcnt lgkmcnt(0)
	v_max3_f32 v199, v195, v84, v85
	v_sub_f32_e32 v85, v93, v199
	v_mul_f32_e32 v85, 0x3fb8aa3b, v85
	v_exp_f32_e32 v101, v85
	v_sub_f32_e32 v85, v194, v199
	v_mul_f32_e32 v85, 0x3fb8aa3b, v85
	v_exp_f32_e32 v179, v85
	v_sub_f32_e32 v85, v180, v199
	v_mul_f32_e32 v85, 0x3fb8aa3b, v85
	v_exp_f32_e32 v103, v85
	v_sub_f32_e32 v85, v178, v199
	v_mul_f32_e32 v85, 0x3fb8aa3b, v85
	v_exp_f32_e32 v183, v85
	v_sub_f32_e32 v85, v196, v199
	v_mul_f32_e32 v85, 0x3fb8aa3b, v85
	v_exp_f32_e32 v180, v85
	v_sub_f32_e32 v85, v182, v199
	v_mul_f32_e32 v85, 0x3fb8aa3b, v85
	v_sub_f32_e32 v84, v195, v199
	v_exp_f32_e32 v195, v85
	v_sub_f32_e32 v85, v200, v199
	v_mul_f32_e32 v84, 0x3fb8aa3b, v84
	v_mul_f32_e32 v85, 0x3fb8aa3b, v85
	v_exp_f32_e32 v184, v85
	v_sub_f32_e32 v85, v197, v199
	v_exp_f32_e32 v197, v84
	v_mul_f32_e32 v85, 0x3fb8aa3b, v85
	v_exp_f32_e32 v196, v85
	v_sub_f32_e32 v85, v102, v199
	v_mul_f32_e32 v85, 0x3fb8aa3b, v85
	v_exp_f32_e32 v102, v85
	v_sub_f32_e32 v85, v201, v199
	ds_bpermute_b32 v200, v136, v197
	ds_bpermute_b32 v201, v146, v197
	ds_bpermute_b32 v202, v147, v197
	ds_bpermute_b32 v203, v135, v197
	v_sub_f32_e32 v82, v82, v199
	v_mul_f32_e32 v82, 0x3fb8aa3b, v82
	v_sub_f32_e32 v83, v83, v199
	v_exp_f32_e32 v194, v82
	v_sub_f32_e32 v82, 0xf149f2ca, v199
	v_mul_f32_e32 v85, 0x3fb8aa3b, v85
	v_mul_f32_e32 v83, 0x3fb8aa3b, v83
	v_mul_f32_e32 v82, 0x3fb8aa3b, v82
	v_exp_f32_e32 v182, v85
	v_exp_f32_e32 v178, v83
	v_exp_f32_e32 v100, v82
	s_waitcnt lgkmcnt(0)
	v_pk_mul_f32 v[84:85], v[52:53], v[202:203]
	v_pk_mul_f32 v[82:83], v[50:51], v[200:201]
	v_pk_mul_f32 v[52:53], v[80:81], v[202:203]
	v_pk_mul_f32 v[50:51], v[78:79], v[200:201]
	v_cvt_pk_bf16_f32 v78, v101, v179
	v_cvt_pk_bf16_f32 v79, v103, v183
	v_cvt_pk_bf16_f32 v80, v180, v195
	v_cvt_pk_bf16_f32 v81, v184, v196
	v_pk_mul_f32 v[56:57], v[56:57], v[202:203]
	v_pk_mul_f32 v[54:55], v[54:55], v[200:201]
	v_pk_mul_f32 v[60:61], v[60:61], v[202:203]
	v_pk_mul_f32 v[58:59], v[58:59], v[200:201]
	v_pk_mul_f32 v[64:65], v[64:65], v[202:203]
	v_pk_mul_f32 v[62:63], v[62:63], v[200:201]
	v_pk_mul_f32 v[68:69], v[68:69], v[202:203]
	v_pk_mul_f32 v[66:67], v[66:67], v[200:201]
	v_pk_mul_f32 v[72:73], v[72:73], v[202:203]
	v_pk_mul_f32 v[70:71], v[70:71], v[200:201]
	v_pk_mul_f32 v[76:77], v[76:77], v[202:203]
	v_pk_mul_f32 v[74:75], v[74:75], v[200:201]
	ds_read_b64_tr_b16 v[202:203], v177 offset:39424
	ds_read_b64_tr_b16 v[200:201], v177 offset:34816
	ds_read_b64_tr_b16 v[204:205], v177 offset:34848
	s_waitcnt lgkmcnt(1)
	v_mfma_f32_16x16x32_bf16 v[82:85], v[78:81], v[200:203], v[82:85]
	ds_read_b64_tr_b16 v[206:207], v177 offset:39456
	ds_read_b64_tr_b16 v[200:201], v177 offset:34880
	ds_read_b64_tr_b16 v[202:203], v177 offset:39488
	v_mov_b32_e32 v93, v87
	s_waitcnt lgkmcnt(0)
	v_mfma_f32_16x16x32_bf16 v[58:61], v[78:81], v[200:203], v[58:61]
	ds_read_b64_tr_b16 v[200:201], v177 offset:34912
	ds_read_b64_tr_b16 v[202:203], v177 offset:39520
	s_waitcnt lgkmcnt(0)
	v_mfma_f32_16x16x32_bf16 v[62:65], v[78:81], v[200:203], v[62:65]
	ds_read_b64_tr_b16 v[200:201], v177 offset:34944
	ds_read_b64_tr_b16 v[202:203], v177 offset:39552
	s_waitcnt lgkmcnt(0)
	v_mfma_f32_16x16x32_bf16 v[66:69], v[78:81], v[200:203], v[66:69]
	ds_read_b64_tr_b16 v[200:201], v177 offset:34976
	ds_read_b64_tr_b16 v[202:203], v177 offset:39584
	s_waitcnt lgkmcnt(0)
	v_mfma_f32_16x16x32_bf16 v[70:73], v[78:81], v[200:203], v[70:73]
	ds_read_b64_tr_b16 v[200:201], v177 offset:35008
	ds_read_b64_tr_b16 v[202:203], v177 offset:39616
	s_waitcnt lgkmcnt(0)
	v_mfma_f32_16x16x32_bf16 v[200:203], v[78:81], v[200:203], v[74:77]
	s_nop 2
	ds_read_b64_tr_b16 v[74:75], v177 offset:35040
	ds_read_b64_tr_b16 v[76:77], v177 offset:39648
	v_mfma_f32_16x16x32_bf16 v[54:57], v[78:81], v[204:207], v[54:57]
	v_cvt_pk_bf16_f32 v206, v100, v100
	v_cvt_pk_bf16_f32 v204, v102, v182
	v_cvt_pk_bf16_f32 v205, v178, v194
	s_waitcnt lgkmcnt(0)
	v_mfma_f32_16x16x32_bf16 v[78:81], v[78:81], v[74:77], v[50:53]
	s_nop 2
	ds_read_b64_tr_b16 v[50:51], v176 offset:34816
	ds_read_b64_tr_b16 v[208:209], v176 offset:34848
	v_mov_b32_e32 v207, v206
	s_waitcnt lgkmcnt(1)
	v_mov_b32_e32 v52, v50
	v_mov_b32_e32 v53, v51
	s_waitcnt lgkmcnt(0)
	v_mov_b32_e32 v210, v208
	v_mov_b32_e32 v211, v209
	v_mfma_f32_16x16x32_bf16 v[74:77], v[204:207], v[50:53], v[82:85]
	s_nop 0
	v_mfma_f32_16x16x32_bf16 v[50:53], v[204:207], v[208:211], v[54:57]
	s_nop 0
	ds_read_b64_tr_b16 v[82:83], v176 offset:35040
	s_waitcnt lgkmcnt(0)
	v_mov_b32_e32 v84, v82
	ds_read_b64_tr_b16 v[54:55], v176 offset:34880
	v_mov_b32_e32 v85, v83
	s_waitcnt lgkmcnt(0)
	v_mov_b32_e32 v56, v54
	v_mov_b32_e32 v57, v55
	v_mfma_f32_16x16x32_bf16 v[78:81], v[204:207], v[82:85], v[78:81]
	s_nop 0
	v_mfma_f32_16x16x32_bf16 v[54:57], v[204:207], v[54:57], v[58:61]
	s_nop 2
	ds_read_b64_tr_b16 v[58:59], v176 offset:34912
	s_waitcnt lgkmcnt(0)
; #define LAS __attribute__((address_space(3)))
; __device__ __forceinline__ void na_fast_unit(int unit, const bf16_t* P, const float* rpb, bf16_t* AO, LAS unsigned char* lds) {
;     ...
;         if (s + 1 < 6) NA_LOAD(s + 1);
;         const bool win = s < 4;
;         f32x4 sc[4];
;         const int kr = rstart + 2 * s + kh;
;         const float* bp = rpb + (h * 15 + (win ? kr - r + 7 : 0)) * 31 - col + 15;
; #pragma unroll
;         for (int j = 0; j < 4; ++j) {
;             if (win && j == 3) { sc[j] = (f32x4){-1.0e30f, -1.0e30f, -1.0e30f, -1.0e30f}; }
;             else { const int lk = 64 * kh + (win ? 16 * (ct0 + j) : 16 * j) + l15;
;                 f32x4 X = (f32x4){0.f, 0.f, 0.f, 0.f};
; #pragma unroll
;                 for (int kk = 0; kk < 4; ++kk) { const bf16x8 kf = *(const LAS bf16x8*)(buf + NA_KB + lk * NA_RSK + (32 * kk + 8 * q) * 2); X = __builtin_amdgcn_mfma_f32_16x16x32_bf16(kf, qf[kk], X, 0, 0, 0); }
;                 if (win) {
; #pragma unroll
;                     for (int rg = 0; rg < 4; ++rg) { const int kc = 16 * (ct0 + j) + 4 * q + rg; const bool ok = kc >= cstart && kc < cstart + 16;
;                         float bias = 0.f; if (ok) bias = bp[kc];
;                         sc[j][rg] = ok ? X[rg] * scale + bias : -1.0e30f; }
	v_mov_b32_e32 v60, v58
	v_mov_b32_e32 v61, v59
	s_nop 1
	v_mfma_f32_16x16x32_bf16 v[58:61], v[204:207], v[58:61], v[62:65]
	s_nop 2
	ds_read_b64_tr_b16 v[62:63], v176 offset:34944
	s_waitcnt lgkmcnt(0)
	v_mov_b32_e32 v64, v62
	v_mov_b32_e32 v65, v63
	s_nop 1
	v_mfma_f32_16x16x32_bf16 v[66:69], v[204:207], v[62:65], v[66:69]
	ds_read_b64_tr_b16 v[62:63], v176 offset:34976
	s_waitcnt lgkmcnt(0)
	v_mov_b32_e32 v64, v62
	v_mov_b32_e32 v65, v63
	s_nop 1
	v_mfma_f32_16x16x32_bf16 v[62:65], v[204:207], v[62:65], v[70:73]
	s_nop 2
	ds_read_b64_tr_b16 v[70:71], v176 offset:35008
	s_waitcnt vmcnt(7)
	ds_write_b128 v139, v[18:21]
	s_waitcnt vmcnt(6)
	ds_write_b128 v140, v[22:25]
	s_waitcnt vmcnt(5)
	ds_write_b128 v141, v[26:29]
	s_waitcnt vmcnt(4)
	ds_write_b128 v142, v[30:33]
	s_waitcnt vmcnt(3)
	ds_write_b128 v139, v[34:37] offset:17408
	s_waitcnt vmcnt(2)
	ds_write_b128 v143, v[38:41]
	s_waitcnt vmcnt(1)
	ds_write_b128 v144, v[42:45]
	s_waitcnt vmcnt(0)
	ds_write_b128 v145, v[46:49]
	v_or_b32_e32 v18, s2, v168
	v_mul_lo_u32 v18, v18, s46
	v_mov_b32_e32 v19, v87
	v_lshl_add_u64 v[18:19], s[54:55], 0, v[18:19]
	v_or_b32_e32 v26, s2, v170
	v_lshl_add_u64 v[18:19], v[18:19], 0, s[24:25]
	v_mul_lo_u32 v26, v26, s46
	v_mov_b32_e32 v27, v87
	v_lshl_add_u64 v[18:19], v[18:19], 0, v[92:93]
	v_lshl_add_u64 v[26:27], s[54:55], 0, v[26:27]
	v_or_b32_e32 v34, s2, v104
	v_lshl_add_u64 v[22:23], v[18:19], 0, s[10:11]
	v_add_co_u32_e32 v18, vcc, s47, v18
	v_lshl_add_u64 v[26:27], v[26:27], 0, s[24:25]
	v_mul_lo_u32 v34, v34, s46
	v_mov_b32_e32 v35, v87
	v_addc_co_u32_e32 v19, vcc, 0, v19, vcc
	v_lshl_add_u64 v[26:27], v[26:27], 0, v[92:93]
	v_lshl_add_u64 v[34:35], s[54:55], 0, v[34:35]
	v_or_b32_e32 v42, s2, v105
	v_lshl_add_u64 v[30:31], v[26:27], 0, s[10:11]
	v_add_co_u32_e32 v26, vcc, s47, v26
	v_lshl_add_u64 v[34:35], v[34:35], 0, s[24:25]
	v_mul_lo_u32 v42, v42, s46
	v_mov_b32_e32 v43, v87
	v_addc_co_u32_e32 v27, vcc, 0, v27, vcc
	v_lshl_add_u64 v[34:35], v[34:35], 0, v[92:93]
	v_lshl_add_u64 v[42:43], s[54:55], 0, v[42:43]
	v_lshl_add_u64 v[38:39], v[34:35], 0, s[10:11]
	v_add_co_u32_e32 v34, vcc, s47, v34
	v_lshl_add_u64 v[42:43], v[42:43], 0, s[24:25]
	s_nop 0
	v_addc_co_u32_e32 v35, vcc, 0, v35, vcc
	v_lshl_add_u64 v[42:43], v[42:43], 0, v[92:93]
	v_lshl_add_u64 v[46:47], v[42:43], 0, s[10:11]
	v_add_co_u32_e32 v42, vcc, s47, v42
	s_waitcnt lgkmcnt(0)
	s_barrier
	s_nop 0
	v_addc_co_u32_e32 v43, vcc, 0, v43, vcc
	v_add_u32_e32 v239, 0, v244
	v_cmp_gt_u32_e32 vcc, 16, v239
	s_and_saveexec_b64 s[86:87], vcc
	global_load_dword v226, v[240:241], off offset:804
	s_or_b64 exec, exec, s[86:87]
	v_add_u32_e32 v239, 1, v244
	v_cmp_gt_u32_e32 vcc, 16, v239
	s_and_saveexec_b64 s[86:87], vcc
	global_load_dword v227, v[240:241], off offset:808
	s_or_b64 exec, exec, s[86:87]
	v_add_u32_e32 v239, 2, v244
	v_cmp_gt_u32_e32 vcc, 16, v239
	s_and_saveexec_b64 s[86:87], vcc
	global_load_dword v229, v[240:241], off offset:812
	s_or_b64 exec, exec, s[86:87]
	v_add_u32_e32 v239, 3, v244
	v_cmp_gt_u32_e32 vcc, 16, v239
	s_and_saveexec_b64 s[86:87], vcc
	global_load_dword v230, v[240:241], off offset:816
	s_or_b64 exec, exec, s[86:87]
	v_add_u32_e32 v239, 16, v244
	v_cmp_gt_u32_e32 vcc, 16, v239
	s_and_saveexec_b64 s[86:87], vcc
	global_load_dword v231, v[240:241], off offset:868
	s_or_b64 exec, exec, s[86:87]
	v_add_u32_e32 v239, 17, v244
	v_cmp_gt_u32_e32 vcc, 16, v239
	s_and_saveexec_b64 s[86:87], vcc
	global_load_dword v232, v[240:241], off offset:872
	s_or_b64 exec, exec, s[86:87]
	v_add_u32_e32 v239, 18, v244
	v_cmp_gt_u32_e32 vcc, 16, v239
	s_and_saveexec_b64 s[86:87], vcc
	global_load_dword v233, v[240:241], off offset:876
	s_or_b64 exec, exec, s[86:87]
	v_add_u32_e32 v239, 19, v244
	v_cmp_gt_u32_e32 vcc, 16, v239
	s_and_saveexec_b64 s[86:87], vcc
	global_load_dword v234, v[240:241], off offset:880
	s_or_b64 exec, exec, s[86:87]
	v_add_u32_e32 v239, 32, v244
	v_cmp_gt_u32_e32 vcc, 16, v239
	s_and_saveexec_b64 s[86:87], vcc
	global_load_dword v235, v[240:241], off offset:932
	s_or_b64 exec, exec, s[86:87]
	v_add_u32_e32 v239, 33, v244
	v_cmp_gt_u32_e32 vcc, 16, v239
	s_and_saveexec_b64 s[86:87], vcc
	global_load_dword v236, v[240:241], off offset:936
	s_or_b64 exec, exec, s[86:87]
	v_add_u32_e32 v239, 34, v244
	v_cmp_gt_u32_e32 vcc, 16, v239
	s_and_saveexec_b64 s[86:87], vcc
	global_load_dword v237, v[240:241], off offset:940
	s_or_b64 exec, exec, s[86:87]
	v_add_u32_e32 v239, 35, v244
	v_cmp_gt_u32_e32 vcc, 16, v239
	s_and_saveexec_b64 s[86:87], vcc
	global_load_dword v238, v[240:241], off offset:944
	s_or_b64 exec, exec, s[86:87]
	global_load_dwordx4 v[18:21], v[18:19], off offset:1024
	s_nop 0
	global_load_dwordx4 v[22:25], v[22:23], off offset:2048
	s_nop 0
	global_load_dwordx4 v[26:29], v[26:27], off offset:1024
	s_nop 0
	global_load_dwordx4 v[30:33], v[30:31], off offset:2048
	s_nop 0
	global_load_dwordx4 v[34:37], v[34:35], off offset:1024
	s_nop 0
	global_load_dwordx4 v[38:41], v[38:39], off offset:2048
	s_nop 0
	global_load_dwordx4 v[42:45], v[42:43], off offset:1024
	s_nop 0
	global_load_dwordx4 v[46:49], v[46:47], off offset:2048
	ds_read_b128 v[82:85], v181
	s_waitcnt lgkmcnt(9)
	v_mov_b32_e32 v72, v70
	v_mov_b32_e32 v73, v71
	s_add_i32 s2, s42, 0xba
	s_ashr_i32 s3, s2, 31
	v_mfma_f32_16x16x32_bf16 v[70:73], v[204:207], v[70:73], v[200:203]
	v_lshl_add_u64 v[98:99], s[2:3], 2, v[98:99]
	v_lshl_add_u64 v[94:95], v[94:95], 2, v[98:99]
	v_mov_b32_e32 v93, 0xf149f2ca
	ds_read_b128 v[200:203], v181 offset:64
	s_waitcnt lgkmcnt(1)
	v_mfma_f32_16x16x32_bf16 v[82:85], v[82:85], v[14:17], 0
	s_waitcnt lgkmcnt(0)
	v_mfma_f32_16x16x32_bf16 v[82:85], v[200:203], v[10:13], v[82:85]
	ds_read_b128 v[200:203], v181 offset:128
	s_waitcnt lgkmcnt(0)
	v_mfma_f32_16x16x32_bf16 v[82:85], v[200:203], v[6:9], v[82:85]
	ds_read_b128 v[200:203], v181 offset:192
	s_waitcnt lgkmcnt(0)
	v_mfma_f32_16x16x32_bf16 v[82:85], v[200:203], v[2:5], v[82:85]
	s_and_saveexec_b64 s[2:3], s[14:15]
	s_cbranch_execz .LBB0_1288
	s_waitcnt vmcnt(8)
	v_mov_b32_e32 v93, v226
	s_nop 3
	v_fmac_f32_e32 v93, 0x3db504f3, v82
; #define LAS __attribute__((address_space(3)))
; __device__ __forceinline__ void na_fast_unit(int unit, const bf16_t* P, const float* rpb, bf16_t* AO, LAS unsigned char* lds) {
;     ...
;         for (int j = 0; j < 4; ++j) {
;             if (win && j == 3) { sc[j] = (f32x4){-1.0e30f, -1.0e30f, -1.0e30f, -1.0e30f}; }
;             else { const int lk = 64 * kh + (win ? 16 * (ct0 + j) : 16 * j) + l15;
;                 f32x4 X = (f32x4){0.f, 0.f, 0.f, 0.f};
; #pragma unroll
;                 for (int kk = 0; kk < 4; ++kk) { const bf16x8 kf = *(const LAS bf16x8*)(buf + NA_KB + lk * NA_RSK + (32 * kk + 8 * q) * 2); X = __builtin_amdgcn_mfma_f32_16x16x32_bf16(kf, qf[kk], X, 0, 0, 0); }
;                 if (win) {
; #pragma unroll
;                     for (int rg = 0; rg < 4; ++rg) { const int kc = 16 * (ct0 + j) + 4 * q + rg; const bool ok = kc >= cstart && kc < cstart + 16;
;                         float bias = 0.f; if (ok) bias = bp[kc];
;                         sc[j][rg] = ok ? X[rg] * scale + bias : -1.0e30f; }
;                 } else sc[j] = X * scale; } }
.LBB0_1288:
	s_or_b64 exec, exec, s[2:3]
	s_and_saveexec_b64 s[2:3], s[16:17]
	s_cbranch_execz .LBB0_1290
	s_waitcnt vmcnt(8)
	v_mov_b32_e32 v198, v227
	s_nop 0
	v_fmac_f32_e32 v198, 0x3db504f3, v83
.LBB0_1290:
	s_or_b64 exec, exec, s[2:3]
	v_mov_b32_e32 v176, 0xf149f2ca
	v_mov_b32_e32 v177, 0xf149f2ca
	s_and_saveexec_b64 s[2:3], s[18:19]
	s_cbranch_execz .LBB0_1292
	s_waitcnt vmcnt(8)
	v_mov_b32_e32 v177, v229
	v_fmac_f32_e32 v177, 0x3db504f3, v84
.LBB0_1292:
	s_or_b64 exec, exec, s[2:3]
	s_and_saveexec_b64 s[2:3], s[20:21]
	s_cbranch_execz .LBB0_1294
	s_waitcnt vmcnt(8)
	v_mov_b32_e32 v176, v230
	v_fmac_f32_e32 v176, 0x3db504f3, v85
.LBB0_1294:
	s_or_b64 exec, exec, s[2:3]
	ds_read_b128 v[82:85], v185
	ds_read_b128 v[200:203], v185 offset:64
	ds_read_b128 v[204:207], v185 offset:128
	v_mov_b32_e32 v181, 0xf149f2ca
	v_lshl_add_u64 v[94:95], v[86:87], 2, v[98:99]
	s_waitcnt lgkmcnt(2)
	v_mfma_f32_16x16x32_bf16 v[82:85], v[82:85], v[14:17], 0
	v_mov_b32_e32 v86, 0xf149f2ca
	s_waitcnt lgkmcnt(1)
	v_mfma_f32_16x16x32_bf16 v[82:85], v[200:203], v[10:13], v[82:85]
	ds_read_b128 v[200:203], v185 offset:192
	s_waitcnt lgkmcnt(1)
	v_mfma_f32_16x16x32_bf16 v[82:85], v[204:207], v[6:9], v[82:85]
	s_waitcnt lgkmcnt(0)
	v_mfma_f32_16x16x32_bf16 v[82:85], v[200:203], v[2:5], v[82:85]
	s_and_saveexec_b64 s[2:3], s[26:27]
	s_cbranch_execz .LBB0_1296
	s_waitcnt vmcnt(8)
	v_mov_b32_e32 v86, v231
	s_nop 3
	v_fmac_f32_e32 v86, 0x3db504f3, v82
.LBB0_1296:
	s_or_b64 exec, exec, s[2:3]
	s_and_saveexec_b64 s[2:3], s[28:29]
	s_cbranch_execz .LBB0_1298
	s_waitcnt vmcnt(8)
	v_mov_b32_e32 v181, v232
	s_nop 0
	v_fmac_f32_e32 v181, 0x3db504f3, v83
.LBB0_1298:
	s_or_b64 exec, exec, s[2:3]
	v_mov_b32_e32 v185, 0xf149f2ca
	v_mov_b32_e32 v200, 0xf149f2ca
	s_and_saveexec_b64 s[2:3], s[30:31]
	s_cbranch_execz .LBB0_1300
	s_waitcnt vmcnt(8)
	v_mov_b32_e32 v200, v233
	v_fmac_f32_e32 v200, 0x3db504f3, v84
.LBB0_1300:
	s_or_b64 exec, exec, s[2:3]
	s_and_saveexec_b64 s[2:3], s[34:35]
	s_cbranch_execz .LBB0_1302
	s_waitcnt vmcnt(8)
	v_mov_b32_e32 v185, v234
	v_fmac_f32_e32 v185, 0x3db504f3, v85
.LBB0_1302:
	s_or_b64 exec, exec, s[2:3]
	ds_read_b128 v[82:85], v191
	ds_read_b128 v[202:205], v191 offset:64
	ds_read_b128 v[206:209], v191 offset:128
	v_lshl_add_u64 v[94:95], v[96:97], 2, v[98:99]
	v_mov_b32_e32 v201, 0xf149f2ca
	s_waitcnt lgkmcnt(2)
	v_mfma_f32_16x16x32_bf16 v[82:85], v[82:85], v[14:17], 0
	s_waitcnt lgkmcnt(1)
	v_mfma_f32_16x16x32_bf16 v[82:85], v[202:205], v[10:13], v[82:85]
	ds_read_b128 v[202:205], v191 offset:192
	v_mov_b32_e32 v191, 0xf149f2ca
	s_waitcnt lgkmcnt(1)
	v_mfma_f32_16x16x32_bf16 v[82:85], v[206:209], v[6:9], v[82:85]
	s_waitcnt lgkmcnt(0)
	v_mfma_f32_16x16x32_bf16 v[82:85], v[202:205], v[2:5], v[82:85]
	s_and_saveexec_b64 s[2:3], s[36:37]
	s_cbranch_execz .LBB0_1304
	s_waitcnt vmcnt(8)
	v_mov_b32_e32 v201, v235
	s_nop 3
	v_fmac_f32_e32 v201, 0x3db504f3, v82
.LBB0_1304:
	s_or_b64 exec, exec, s[2:3]
	s_and_saveexec_b64 s[2:3], s[38:39]
	s_cbranch_execz .LBB0_1306
	s_waitcnt vmcnt(8)
	v_mov_b32_e32 v191, v236
	s_nop 0
	v_fmac_f32_e32 v191, 0x3db504f3, v83
